# DSA top-256 select: interpolation (Illinois) search for the 256-count threshold before falling back to bitwise bisection
# baseline (speedup 1.0000x reference)
.LBB0_740:
	s_andn2_b64 vcc, exec, s[0:1]
	s_cbranch_vccnz .LBB0_2599
	ds_read2st64_b32 v[62:63], v183 offset1:1
	ds_read2st64_b32 v[60:61], v183 offset0:2 offset1:3
	ds_read2st64_b32 v[58:59], v183 offset0:4 offset1:5
	ds_read2st64_b32 v[56:57], v183 offset0:6 offset1:7
	s_ashr_i32 s0, s40, 6
	s_add_i32 s0, s0, 8
	s_ashr_i32 s2, s0, 3
	v_writelane_b32 v254, s2, 52
	s_cmp_lt_i32 s2, 4
	s_mov_b64 s[2:3], 0
	v_writelane_b32 v254, s2, 54
	s_mov_b64 s[0:1], -1
	s_nop 0
	v_writelane_b32 v254, s3, 55
	s_cbranch_scc1 .LBB0_1861
	v_readlane_b32 s0, v254, 52
	s_cmp_gt_i32 s0, 5
	s_cbranch_scc0 .LBB0_749
	s_cmp_gt_i32 s0, 6
	s_cbranch_scc0 .LBB0_750
	s_cmp_eq_u32 s0, 7
	s_mov_b64 s[0:1], -1
	s_cbranch_scc0 .LBB0_1097
	s_waitcnt lgkmcnt(3)
	v_max_u32_e32 v89, v63, v62
	s_waitcnt lgkmcnt(2)
	v_max3_u32 v89, v61, v60, v89
	s_waitcnt lgkmcnt(1)
	v_max3_u32 v89, v59, v58, v89
	s_waitcnt lgkmcnt(0)
	v_max3_u32 v89, v57, v56, v89
	ds_read2st64_b32 v[112:113], v183 offset0:8 offset1:9
	ds_read2st64_b32 v[110:111], v183 offset0:10 offset1:11
	ds_read2st64_b32 v[108:109], v183 offset0:12 offset1:13
	ds_read2st64_b32 v[106:107], v183 offset0:14 offset1:15
	ds_read2st64_b32 v[104:105], v183 offset0:16 offset1:17
	ds_read2st64_b32 v[102:103], v183 offset0:18 offset1:19
	ds_read2st64_b32 v[100:101], v183 offset0:20 offset1:21
	ds_read2st64_b32 v[98:99], v183 offset0:22 offset1:23
	ds_read2st64_b32 v[96:97], v183 offset0:24 offset1:25
	ds_read2st64_b32 v[94:95], v183 offset0:26 offset1:27
	ds_read2st64_b32 v[92:93], v183 offset0:28 offset1:29
	ds_read2st64_b32 v[90:91], v183 offset0:30 offset1:31
	ds_read2st64_b32 v[86:87], v183 offset0:32 offset1:33
	ds_read2st64_b32 v[84:85], v183 offset0:34 offset1:35
	ds_read2st64_b32 v[82:83], v183 offset0:36 offset1:37
	ds_read2st64_b32 v[80:81], v183 offset0:38 offset1:39
	ds_read2st64_b32 v[78:79], v183 offset0:40 offset1:41
	ds_read2st64_b32 v[76:77], v183 offset0:42 offset1:43
	ds_read2st64_b32 v[74:75], v183 offset0:44 offset1:45
	ds_read2st64_b32 v[72:73], v183 offset0:46 offset1:47
	ds_read2st64_b32 v[70:71], v183 offset0:48 offset1:49
	ds_read2st64_b32 v[68:69], v183 offset0:50 offset1:51
	ds_read2st64_b32 v[66:67], v183 offset0:52 offset1:53
	ds_read2st64_b32 v[64:65], v183 offset0:54 offset1:55
	s_waitcnt lgkmcnt(14)
	v_max3_u32 v89, v113, v112, v89
	v_max3_u32 v89, v111, v110, v89
	v_max3_u32 v89, v109, v108, v89
	v_max3_u32 v89, v107, v106, v89
	v_max3_u32 v89, v105, v104, v89
	v_max3_u32 v89, v103, v102, v89
	v_max3_u32 v89, v101, v100, v89
	v_max3_u32 v89, v99, v98, v89
	v_max3_u32 v89, v97, v96, v89
	v_max3_u32 v89, v95, v94, v89
	s_waitcnt lgkmcnt(13)
	v_max3_u32 v89, v93, v92, v89
	s_waitcnt lgkmcnt(12)
	v_max3_u32 v89, v91, v90, v89
	s_waitcnt lgkmcnt(11)
	v_max3_u32 v89, v87, v86, v89
	s_waitcnt lgkmcnt(10)
	v_max3_u32 v89, v85, v84, v89
	s_waitcnt lgkmcnt(9)
	v_max3_u32 v89, v83, v82, v89
	s_waitcnt lgkmcnt(8)
	v_max3_u32 v89, v81, v80, v89
	s_waitcnt lgkmcnt(7)
	v_max3_u32 v89, v79, v78, v89
	s_waitcnt lgkmcnt(6)
	v_max3_u32 v89, v77, v76, v89
	s_waitcnt lgkmcnt(5)
	v_max3_u32 v89, v75, v74, v89
	s_waitcnt lgkmcnt(4)
	v_max3_u32 v89, v73, v72, v89
	s_waitcnt lgkmcnt(3)
	v_max3_u32 v89, v71, v70, v89
	s_waitcnt lgkmcnt(2)
	v_max3_u32 v89, v69, v68, v89
	s_waitcnt lgkmcnt(1)
	v_max3_u32 v89, v67, v66, v89
	s_waitcnt lgkmcnt(0)
	v_max3_u32 v89, v65, v64, v89
	s_nop 1
	v_max_u32_dpp v89, v89, v89 quad_perm:[1,0,3,2] row_mask:0xf bank_mask:0xf bound_ctrl:1
	s_nop 1
	v_max_u32_dpp v89, v89, v89 quad_perm:[2,3,0,1] row_mask:0xf bank_mask:0xf bound_ctrl:1
	s_nop 1
	v_max_u32_dpp v89, v89, v89 row_half_mirror row_mask:0xf bank_mask:0xf bound_ctrl:1
	s_nop 1
	v_max_u32_dpp v89, v89, v89 row_mirror row_mask:0xf bank_mask:0xf bound_ctrl:1
	v_mov_b32_e32 v114, v89
	s_nop 1
	v_permlane16_swap_b32_e32 v89, v114
	v_max_u32_e32 v89, v89, v114
	v_mov_b32_e32 v114, v89
	s_nop 1
	v_permlane32_swap_b32_e32 v89, v114
	v_max_u32_e32 v89, v89, v114
	s_nop 0
	v_readfirstlane_b32 s0, v89
	s_and_b32 s7, s0, 0xff800000
	s_lshr_b32 s0, s0, 23
	s_min_u32 s0, s0, 3
	s_mov_b32 s21, 0
	s_add_i32 s5, s0, 1
	s_branch .LBB0_747

.LBB0_747:
	v_mov_b32_e32 v114, v199
	v_mov_b32_e32 v115, v199
	s_mov_b32 s4, s7
	v_mov_b32_e32 v89, s7
	v_cmp_ge_u32_e64 s[0:1], v62, v89
	v_cmp_ge_u32_e64 s[2:3], v63, v89
	v_cmp_ge_u32_e64 s[6:7], v60, v89
	v_cmp_ge_u32_e64 s[8:9], v61, v89
	v_cmp_ge_u32_e64 s[10:11], v58, v89
	v_cmp_ge_u32_e64 s[12:13], v59, v89
	v_cmp_ge_u32_e64 s[14:15], v56, v89
	v_cmp_ge_u32_e64 s[16:17], v57, v89
	v_addc_co_u32_e64 v114, s[0:1], v114, 0, s[0:1]
	v_addc_co_u32_e64 v115, s[2:3], v115, 0, s[2:3]
	v_addc_co_u32_e64 v114, s[6:7], v114, 0, s[6:7]
	v_addc_co_u32_e64 v115, s[8:9], v115, 0, s[8:9]
	v_addc_co_u32_e64 v114, s[10:11], v114, 0, s[10:11]
	v_addc_co_u32_e64 v115, s[12:13], v115, 0, s[12:13]
	v_addc_co_u32_e64 v114, s[14:15], v114, 0, s[14:15]
	v_addc_co_u32_e64 v115, s[16:17], v115, 0, s[16:17]
	s_nop 0
	v_cmp_ge_u32_e64 s[0:1], v112, v89
	v_cmp_ge_u32_e64 s[2:3], v113, v89
	v_cmp_ge_u32_e64 s[6:7], v110, v89
	v_cmp_ge_u32_e64 s[8:9], v111, v89
	v_cmp_ge_u32_e64 s[10:11], v108, v89
	v_cmp_ge_u32_e64 s[12:13], v109, v89
	v_cmp_ge_u32_e64 s[14:15], v106, v89
	v_cmp_ge_u32_e64 s[16:17], v107, v89
	v_addc_co_u32_e64 v114, s[0:1], v114, 0, s[0:1]
	v_addc_co_u32_e64 v115, s[2:3], v115, 0, s[2:3]
	v_addc_co_u32_e64 v114, s[6:7], v114, 0, s[6:7]
	v_addc_co_u32_e64 v115, s[8:9], v115, 0, s[8:9]
	v_addc_co_u32_e64 v114, s[10:11], v114, 0, s[10:11]
	v_addc_co_u32_e64 v115, s[12:13], v115, 0, s[12:13]
	v_addc_co_u32_e64 v114, s[14:15], v114, 0, s[14:15]
	v_addc_co_u32_e64 v115, s[16:17], v115, 0, s[16:17]
	s_nop 0
	v_cmp_ge_u32_e64 s[0:1], v104, v89
	v_cmp_ge_u32_e64 s[2:3], v105, v89
	v_cmp_ge_u32_e64 s[6:7], v102, v89
	v_cmp_ge_u32_e64 s[8:9], v103, v89
	v_cmp_ge_u32_e64 s[10:11], v100, v89
	v_cmp_ge_u32_e64 s[12:13], v101, v89
	v_cmp_ge_u32_e64 s[14:15], v98, v89
	v_cmp_ge_u32_e64 s[16:17], v99, v89
	v_addc_co_u32_e64 v114, s[0:1], v114, 0, s[0:1]
	v_addc_co_u32_e64 v115, s[2:3], v115, 0, s[2:3]
	v_addc_co_u32_e64 v114, s[6:7], v114, 0, s[6:7]
	v_addc_co_u32_e64 v115, s[8:9], v115, 0, s[8:9]
	v_addc_co_u32_e64 v114, s[10:11], v114, 0, s[10:11]
	v_addc_co_u32_e64 v115, s[12:13], v115, 0, s[12:13]
	v_addc_co_u32_e64 v114, s[14:15], v114, 0, s[14:15]
	v_addc_co_u32_e64 v115, s[16:17], v115, 0, s[16:17]
	s_nop 0
	v_cmp_ge_u32_e64 s[0:1], v96, v89
	v_cmp_ge_u32_e64 s[2:3], v97, v89
	v_cmp_ge_u32_e64 s[6:7], v94, v89
	v_cmp_ge_u32_e64 s[8:9], v95, v89
	v_cmp_ge_u32_e64 s[10:11], v92, v89
	v_cmp_ge_u32_e64 s[12:13], v93, v89
	v_cmp_ge_u32_e64 s[14:15], v90, v89
	v_cmp_ge_u32_e64 s[16:17], v91, v89
	v_addc_co_u32_e64 v114, s[0:1], v114, 0, s[0:1]
	v_addc_co_u32_e64 v115, s[2:3], v115, 0, s[2:3]
	v_addc_co_u32_e64 v114, s[6:7], v114, 0, s[6:7]
	v_addc_co_u32_e64 v115, s[8:9], v115, 0, s[8:9]
	v_addc_co_u32_e64 v114, s[10:11], v114, 0, s[10:11]
	v_addc_co_u32_e64 v115, s[12:13], v115, 0, s[12:13]
	v_addc_co_u32_e64 v114, s[14:15], v114, 0, s[14:15]
	v_addc_co_u32_e64 v115, s[16:17], v115, 0, s[16:17]
	s_nop 0
	v_cmp_ge_u32_e64 s[0:1], v86, v89
	v_cmp_ge_u32_e64 s[2:3], v87, v89
	v_cmp_ge_u32_e64 s[6:7], v84, v89
	v_cmp_ge_u32_e64 s[8:9], v85, v89
	v_cmp_ge_u32_e64 s[10:11], v82, v89
	v_cmp_ge_u32_e64 s[12:13], v83, v89
	v_cmp_ge_u32_e64 s[14:15], v80, v89
	v_cmp_ge_u32_e64 s[16:17], v81, v89
	v_addc_co_u32_e64 v114, s[0:1], v114, 0, s[0:1]
	v_addc_co_u32_e64 v115, s[2:3], v115, 0, s[2:3]
	v_addc_co_u32_e64 v114, s[6:7], v114, 0, s[6:7]
	v_addc_co_u32_e64 v115, s[8:9], v115, 0, s[8:9]
	v_addc_co_u32_e64 v114, s[10:11], v114, 0, s[10:11]
	v_addc_co_u32_e64 v115, s[12:13], v115, 0, s[12:13]
	v_addc_co_u32_e64 v114, s[14:15], v114, 0, s[14:15]
	v_addc_co_u32_e64 v115, s[16:17], v115, 0, s[16:17]
	s_nop 0
	v_cmp_ge_u32_e64 s[0:1], v78, v89
	v_cmp_ge_u32_e64 s[2:3], v79, v89
	v_cmp_ge_u32_e64 s[6:7], v76, v89
	v_cmp_ge_u32_e64 s[8:9], v77, v89
	v_cmp_ge_u32_e64 s[10:11], v74, v89
	v_cmp_ge_u32_e64 s[12:13], v75, v89
	v_cmp_ge_u32_e64 s[14:15], v72, v89
	v_cmp_ge_u32_e64 s[16:17], v73, v89
	v_addc_co_u32_e64 v114, s[0:1], v114, 0, s[0:1]
	v_addc_co_u32_e64 v115, s[2:3], v115, 0, s[2:3]
	v_addc_co_u32_e64 v114, s[6:7], v114, 0, s[6:7]
	v_addc_co_u32_e64 v115, s[8:9], v115, 0, s[8:9]
	v_addc_co_u32_e64 v114, s[10:11], v114, 0, s[10:11]
	v_addc_co_u32_e64 v115, s[12:13], v115, 0, s[12:13]
	v_addc_co_u32_e64 v114, s[14:15], v114, 0, s[14:15]
	v_addc_co_u32_e64 v115, s[16:17], v115, 0, s[16:17]
	s_nop 0
	v_cmp_ge_u32_e64 s[0:1], v70, v89
	v_cmp_ge_u32_e64 s[2:3], v71, v89
	v_cmp_ge_u32_e64 s[6:7], v68, v89
	v_cmp_ge_u32_e64 s[8:9], v69, v89
	v_cmp_ge_u32_e64 s[10:11], v66, v89
	v_cmp_ge_u32_e64 s[12:13], v67, v89
	v_cmp_ge_u32_e64 s[14:15], v64, v89
	v_cmp_ge_u32_e64 s[16:17], v65, v89
	v_addc_co_u32_e64 v114, s[0:1], v114, 0, s[0:1]
	v_addc_co_u32_e64 v115, s[2:3], v115, 0, s[2:3]
	v_addc_co_u32_e64 v114, s[6:7], v114, 0, s[6:7]
	v_addc_co_u32_e64 v115, s[8:9], v115, 0, s[8:9]
	v_addc_co_u32_e64 v114, s[10:11], v114, 0, s[10:11]
	v_addc_co_u32_e64 v115, s[12:13], v115, 0, s[12:13]
	v_addc_co_u32_e64 v114, s[14:15], v114, 0, s[14:15]
	v_addc_co_u32_e64 v115, s[16:17], v115, 0, s[16:17]
	s_mov_b64 s[0:1], -1
	v_add_u32_e32 v89, v114, v115
	s_mov_b64 s[2:3], -1
	s_nop 0
	v_add_u32_dpp v89, v89, v89 quad_perm:[1,0,3,2] row_mask:0xf bank_mask:0xf bound_ctrl:1
	s_nop 1
	v_add_u32_dpp v89, v89, v89 quad_perm:[2,3,0,1] row_mask:0xf bank_mask:0xf bound_ctrl:1
	s_nop 1
	v_add_u32_dpp v89, v89, v89 row_half_mirror row_mask:0xf bank_mask:0xf bound_ctrl:1
	s_nop 1
	v_add_u32_dpp v89, v89, v89 row_mirror row_mask:0xf bank_mask:0xf bound_ctrl:1
	v_mov_b32_e32 v114, v89
	s_nop 1
	v_permlane16_swap_b32_e32 v89, v114
	v_add_u32_e32 v89, v89, v114
	v_mov_b32_e32 v114, v89
	s_nop 1
	v_permlane32_swap_b32_e32 v89, v114
	v_add_u32_e32 v89, v89, v114
	s_nop 0
	v_readfirstlane_b32 s6, v89
	s_cmpk_lt_i32 s6, 0x100
	s_cbranch_scc0 .LBB0_746
	s_mov_b32 s21, s6
	s_add_i32 s5, s5, -1
	s_add_i32 s7, s4, 0xff800000
	s_cmp_eq_u32 s5, 0
	s_mov_b64 s[0:1], 0
	s_cselect_b64 s[2:3], -1, 0
	s_branch .LBB0_746

.Lsf755_entry:
	s_mov_b32 s20, s4
	s_add_i32 s22, s4, 0x800000
	s_mov_b32 s23, s6
	s_movk_i32 s24, 10
	s_mov_b32 s31, 0
.Lsf755_loop:
	s_sub_i32 s25, s22, s20
	s_cmp_lt_u32 s25, 2
	s_cbranch_scc1 .Lsf755_tie
	s_sub_i32 s26, s23, s21
	s_sub_i32 s27, s23, 0x100
	v_cvt_f32_u32_e32 v116, s25
	v_cvt_f32_u32_e32 v117, s26
	v_cvt_f32_u32_e32 v115, s27
	v_rcp_f32_e32 v117, v117
	v_add_f32_e32 v115, 0.5, v115
	s_nop 0
	v_mul_f32_e32 v116, v116, v117
	v_mul_f32_e32 v115, v115, v116
	v_cvt_u32_f32_e32 v115, v115
	s_nop 0
	v_readfirstlane_b32 s27, v115
	s_sub_i32 s28, s25, 1
	s_max_u32 s27, s27, 1
	s_min_u32 s27, s27, s28
	s_add_i32 s27, s20, s27
	v_mov_b32_e32 v115, s27
	v_mov_b32_e32 v116, v199
	v_mov_b32_e32 v117, v199
	v_cmp_ge_u32_e64 s[2:3], v62, v115
	v_cmp_ge_u32_e64 s[4:5], v63, v115
	v_cmp_ge_u32_e64 s[6:7], v60, v115
	v_cmp_ge_u32_e64 s[8:9], v61, v115
	v_cmp_ge_u32_e64 s[10:11], v58, v115
	v_cmp_ge_u32_e64 s[12:13], v59, v115
	v_cmp_ge_u32_e64 s[14:15], v56, v115
	v_cmp_ge_u32_e64 s[16:17], v57, v115
	v_addc_co_u32_e64 v116, s[2:3], v116, 0, s[2:3]
	v_addc_co_u32_e64 v117, s[4:5], v117, 0, s[4:5]
	v_addc_co_u32_e64 v116, s[6:7], v116, 0, s[6:7]
	v_addc_co_u32_e64 v117, s[8:9], v117, 0, s[8:9]
	v_addc_co_u32_e64 v116, s[10:11], v116, 0, s[10:11]
	v_addc_co_u32_e64 v117, s[12:13], v117, 0, s[12:13]
	v_addc_co_u32_e64 v116, s[14:15], v116, 0, s[14:15]
	v_addc_co_u32_e64 v117, s[16:17], v117, 0, s[16:17]
	s_nop 0
	v_cmp_ge_u32_e64 s[2:3], v112, v115
	v_cmp_ge_u32_e64 s[4:5], v113, v115
	v_cmp_ge_u32_e64 s[6:7], v110, v115
	v_cmp_ge_u32_e64 s[8:9], v111, v115
	v_cmp_ge_u32_e64 s[10:11], v108, v115
	v_cmp_ge_u32_e64 s[12:13], v109, v115
	v_cmp_ge_u32_e64 s[14:15], v106, v115
	v_cmp_ge_u32_e64 s[16:17], v107, v115
	v_addc_co_u32_e64 v116, s[2:3], v116, 0, s[2:3]
	v_addc_co_u32_e64 v117, s[4:5], v117, 0, s[4:5]
	v_addc_co_u32_e64 v116, s[6:7], v116, 0, s[6:7]
	v_addc_co_u32_e64 v117, s[8:9], v117, 0, s[8:9]
	v_addc_co_u32_e64 v116, s[10:11], v116, 0, s[10:11]
	v_addc_co_u32_e64 v117, s[12:13], v117, 0, s[12:13]
	v_addc_co_u32_e64 v116, s[14:15], v116, 0, s[14:15]
	v_addc_co_u32_e64 v117, s[16:17], v117, 0, s[16:17]
	s_nop 0
	v_cmp_ge_u32_e64 s[2:3], v104, v115
	v_cmp_ge_u32_e64 s[4:5], v105, v115
	v_cmp_ge_u32_e64 s[6:7], v102, v115
	v_cmp_ge_u32_e64 s[8:9], v103, v115
	v_cmp_ge_u32_e64 s[10:11], v100, v115
	v_cmp_ge_u32_e64 s[12:13], v101, v115
	v_cmp_ge_u32_e64 s[14:15], v98, v115
	v_cmp_ge_u32_e64 s[16:17], v99, v115
	v_addc_co_u32_e64 v116, s[2:3], v116, 0, s[2:3]
	v_addc_co_u32_e64 v117, s[4:5], v117, 0, s[4:5]
	v_addc_co_u32_e64 v116, s[6:7], v116, 0, s[6:7]
	v_addc_co_u32_e64 v117, s[8:9], v117, 0, s[8:9]
	v_addc_co_u32_e64 v116, s[10:11], v116, 0, s[10:11]
	v_addc_co_u32_e64 v117, s[12:13], v117, 0, s[12:13]
	v_addc_co_u32_e64 v116, s[14:15], v116, 0, s[14:15]
	v_addc_co_u32_e64 v117, s[16:17], v117, 0, s[16:17]
	s_nop 0
	v_cmp_ge_u32_e64 s[2:3], v96, v115
	v_cmp_ge_u32_e64 s[4:5], v97, v115
	v_cmp_ge_u32_e64 s[6:7], v94, v115
	v_cmp_ge_u32_e64 s[8:9], v95, v115
	v_cmp_ge_u32_e64 s[10:11], v92, v115
	v_cmp_ge_u32_e64 s[12:13], v93, v115
	v_cmp_ge_u32_e64 s[14:15], v90, v115
	v_cmp_ge_u32_e64 s[16:17], v91, v115
	v_addc_co_u32_e64 v116, s[2:3], v116, 0, s[2:3]
	v_addc_co_u32_e64 v117, s[4:5], v117, 0, s[4:5]
	v_addc_co_u32_e64 v116, s[6:7], v116, 0, s[6:7]
	v_addc_co_u32_e64 v117, s[8:9], v117, 0, s[8:9]
	v_addc_co_u32_e64 v116, s[10:11], v116, 0, s[10:11]
	v_addc_co_u32_e64 v117, s[12:13], v117, 0, s[12:13]
	v_addc_co_u32_e64 v116, s[14:15], v116, 0, s[14:15]
	v_addc_co_u32_e64 v117, s[16:17], v117, 0, s[16:17]
	s_nop 0
	v_cmp_ge_u32_e64 s[2:3], v86, v115
	v_cmp_ge_u32_e64 s[4:5], v87, v115
	v_cmp_ge_u32_e64 s[6:7], v84, v115
	v_cmp_ge_u32_e64 s[8:9], v85, v115
	v_cmp_ge_u32_e64 s[10:11], v82, v115
	v_cmp_ge_u32_e64 s[12:13], v83, v115
	v_cmp_ge_u32_e64 s[14:15], v80, v115
	v_cmp_ge_u32_e64 s[16:17], v81, v115
	v_addc_co_u32_e64 v116, s[2:3], v116, 0, s[2:3]
	v_addc_co_u32_e64 v117, s[4:5], v117, 0, s[4:5]
	v_addc_co_u32_e64 v116, s[6:7], v116, 0, s[6:7]
	v_addc_co_u32_e64 v117, s[8:9], v117, 0, s[8:9]
	v_addc_co_u32_e64 v116, s[10:11], v116, 0, s[10:11]
	v_addc_co_u32_e64 v117, s[12:13], v117, 0, s[12:13]
	v_addc_co_u32_e64 v116, s[14:15], v116, 0, s[14:15]
	v_addc_co_u32_e64 v117, s[16:17], v117, 0, s[16:17]
	s_nop 0
	v_cmp_ge_u32_e64 s[2:3], v78, v115
	v_cmp_ge_u32_e64 s[4:5], v79, v115
	v_cmp_ge_u32_e64 s[6:7], v76, v115
	v_cmp_ge_u32_e64 s[8:9], v77, v115
	v_cmp_ge_u32_e64 s[10:11], v74, v115
	v_cmp_ge_u32_e64 s[12:13], v75, v115
	v_cmp_ge_u32_e64 s[14:15], v72, v115
	v_cmp_ge_u32_e64 s[16:17], v73, v115
	v_addc_co_u32_e64 v116, s[2:3], v116, 0, s[2:3]
	v_addc_co_u32_e64 v117, s[4:5], v117, 0, s[4:5]
	v_addc_co_u32_e64 v116, s[6:7], v116, 0, s[6:7]
	v_addc_co_u32_e64 v117, s[8:9], v117, 0, s[8:9]
	v_addc_co_u32_e64 v116, s[10:11], v116, 0, s[10:11]
	v_addc_co_u32_e64 v117, s[12:13], v117, 0, s[12:13]
	v_addc_co_u32_e64 v116, s[14:15], v116, 0, s[14:15]
	v_addc_co_u32_e64 v117, s[16:17], v117, 0, s[16:17]
	s_nop 0
	v_cmp_ge_u32_e64 s[2:3], v70, v115
	v_cmp_ge_u32_e64 s[4:5], v71, v115
	v_cmp_ge_u32_e64 s[6:7], v68, v115
	v_cmp_ge_u32_e64 s[8:9], v69, v115
	v_cmp_ge_u32_e64 s[10:11], v66, v115
	v_cmp_ge_u32_e64 s[12:13], v67, v115
	v_cmp_ge_u32_e64 s[14:15], v64, v115
	v_cmp_ge_u32_e64 s[16:17], v65, v115
	v_addc_co_u32_e64 v116, s[2:3], v116, 0, s[2:3]
	v_addc_co_u32_e64 v117, s[4:5], v117, 0, s[4:5]
	v_addc_co_u32_e64 v116, s[6:7], v116, 0, s[6:7]
	v_addc_co_u32_e64 v117, s[8:9], v117, 0, s[8:9]
	v_addc_co_u32_e64 v116, s[10:11], v116, 0, s[10:11]
	v_addc_co_u32_e64 v117, s[12:13], v117, 0, s[12:13]
	v_addc_co_u32_e64 v116, s[14:15], v116, 0, s[14:15]
	v_addc_co_u32_e64 v117, s[16:17], v117, 0, s[16:17]
	s_nop 0
	v_add_u32_e32 v116, v116, v117
	s_nop 1
	v_add_u32_dpp v116, v116, v116 quad_perm:[1,0,3,2] row_mask:0xf bank_mask:0xf bound_ctrl:1
	s_nop 1
	v_add_u32_dpp v116, v116, v116 quad_perm:[2,3,0,1] row_mask:0xf bank_mask:0xf bound_ctrl:1
	s_nop 1
	v_add_u32_dpp v116, v116, v116 row_half_mirror row_mask:0xf bank_mask:0xf bound_ctrl:1
	s_nop 1
	v_add_u32_dpp v116, v116, v116 row_mirror row_mask:0xf bank_mask:0xf bound_ctrl:1
	v_mov_b32_e32 v117, v116
	s_nop 1
	v_permlane16_swap_b32_e32 v116, v117
	v_add_u32_e32 v116, v116, v117
	v_mov_b32_e32 v117, v116
	s_nop 1
	v_permlane32_swap_b32_e32 v116, v117
	v_add_u32_e32 v116, v116, v117
	s_nop 0
	v_readfirstlane_b32 s29, v116
	s_cmpk_eq_i32 s29, 0x100
	s_cbranch_scc1 .Lsf755_hit
	s_cmpk_gt_i32 s29, 0x100
	s_cbranch_scc1 .Lsf755_up
	s_mov_b32 s22, s27
	s_mov_b32 s21, s29
	s_cmp_eq_u32 s31, 2
	s_cbranch_scc0 .Lsf755_hd
	s_sub_i32 s26, s23, 0x100
	s_lshr_b32 s26, s26, 1
	s_max_u32 s26, s26, 1
	s_add_i32 s23, s26, 0x100
.Lsf755_hd:
	s_mov_b32 s31, 2
	s_branch .Lsf755_next
.Lsf755_up:
	s_mov_b32 s20, s27
	s_mov_b32 s23, s29
	s_cmp_eq_u32 s31, 1
	s_cbranch_scc0 .Lsf755_ld
	s_sub_i32 s26, 0x100, s21
	s_lshr_b32 s26, s26, 1
	s_max_u32 s26, s26, 1
	s_sub_i32 s21, 0x100, s26
.Lsf755_ld:
	s_mov_b32 s31, 1
.Lsf755_next:
	s_add_i32 s24, s24, -1
	s_cmp_lg_u32 s24, 0
	s_cbranch_scc1 .Lsf755_loop
	s_sub_i32 s25, s22, s20
	s_cmp_lt_u32 s25, 2
	s_cbranch_scc1 .Lsf755_tie
	s_add_i32 s28, s22, -1
	s_xor_b32 s28, s28, s20
	s_flbit_i32_b32 s29, s28
	s_sub_i32 s5, 31, s29
	s_lshl_b32 s28, 2, s5
	s_add_i32 s28, s28, -1
	s_andn2_b32 s4, s20, s28
	s_branch .LBB0_754
.Lsf755_tie:
	v_mov_b32_e32 v89, s20
	s_mov_b64 s[0:1], 0
	s_branch .LBB0_756
.Lsf755_hit:
	v_mov_b32_e32 v89, s27
	s_mov_b64 s[0:1], -1
	s_branch .LBB0_756

.LBB0_1098:
	s_waitcnt lgkmcnt(3)
	v_max_u32_e32 v89, v63, v62
	s_waitcnt lgkmcnt(2)
	v_max3_u32 v89, v61, v60, v89
	s_waitcnt lgkmcnt(1)
	v_max3_u32 v89, v59, v58, v89
	s_waitcnt lgkmcnt(0)
	v_max3_u32 v89, v57, v56, v89
	ds_read2st64_b32 v[104:105], v183 offset0:8 offset1:9
	ds_read2st64_b32 v[102:103], v183 offset0:10 offset1:11
	ds_read2st64_b32 v[100:101], v183 offset0:12 offset1:13
	ds_read2st64_b32 v[98:99], v183 offset0:14 offset1:15
	ds_read2st64_b32 v[96:97], v183 offset0:16 offset1:17
	ds_read2st64_b32 v[94:95], v183 offset0:18 offset1:19
	ds_read2st64_b32 v[92:93], v183 offset0:20 offset1:21
	ds_read2st64_b32 v[90:91], v183 offset0:22 offset1:23
	ds_read2st64_b32 v[86:87], v183 offset0:24 offset1:25
	ds_read2st64_b32 v[84:85], v183 offset0:26 offset1:27
	ds_read2st64_b32 v[82:83], v183 offset0:28 offset1:29
	ds_read2st64_b32 v[80:81], v183 offset0:30 offset1:31
	ds_read2st64_b32 v[78:79], v183 offset0:32 offset1:33
	ds_read2st64_b32 v[76:77], v183 offset0:34 offset1:35
	ds_read2st64_b32 v[74:75], v183 offset0:36 offset1:37
	ds_read2st64_b32 v[72:73], v183 offset0:38 offset1:39
	ds_read2st64_b32 v[70:71], v183 offset0:40 offset1:41
	ds_read2st64_b32 v[68:69], v183 offset0:42 offset1:43
	ds_read2st64_b32 v[66:67], v183 offset0:44 offset1:45
	ds_read2st64_b32 v[64:65], v183 offset0:46 offset1:47
	s_waitcnt lgkmcnt(14)
	v_max3_u32 v89, v105, v104, v89
	v_max3_u32 v89, v103, v102, v89
	v_max3_u32 v89, v101, v100, v89
	v_max3_u32 v89, v99, v98, v89
	v_max3_u32 v89, v97, v96, v89
	v_max3_u32 v89, v95, v94, v89
	s_waitcnt lgkmcnt(13)
	v_max3_u32 v89, v93, v92, v89
	s_waitcnt lgkmcnt(12)
	v_max3_u32 v89, v91, v90, v89
	s_waitcnt lgkmcnt(11)
	v_max3_u32 v89, v87, v86, v89
	s_waitcnt lgkmcnt(10)
	v_max3_u32 v89, v85, v84, v89
	s_waitcnt lgkmcnt(9)
	v_max3_u32 v89, v83, v82, v89
	s_waitcnt lgkmcnt(8)
	v_max3_u32 v89, v81, v80, v89
	s_waitcnt lgkmcnt(7)
	v_max3_u32 v89, v79, v78, v89
	s_waitcnt lgkmcnt(6)
	v_max3_u32 v89, v77, v76, v89
	s_waitcnt lgkmcnt(5)
	v_max3_u32 v89, v75, v74, v89
	s_waitcnt lgkmcnt(4)
	v_max3_u32 v89, v73, v72, v89
	s_waitcnt lgkmcnt(3)
	v_max3_u32 v89, v71, v70, v89
	s_waitcnt lgkmcnt(2)
	v_max3_u32 v89, v69, v68, v89
	s_waitcnt lgkmcnt(1)
	v_max3_u32 v89, v67, v66, v89
	s_waitcnt lgkmcnt(0)
	v_max3_u32 v89, v65, v64, v89
	s_nop 1
	v_max_u32_dpp v89, v89, v89 quad_perm:[1,0,3,2] row_mask:0xf bank_mask:0xf bound_ctrl:1
	s_nop 1
	v_max_u32_dpp v89, v89, v89 quad_perm:[2,3,0,1] row_mask:0xf bank_mask:0xf bound_ctrl:1
	s_nop 1
	v_max_u32_dpp v89, v89, v89 row_half_mirror row_mask:0xf bank_mask:0xf bound_ctrl:1
	s_nop 1
	v_max_u32_dpp v89, v89, v89 row_mirror row_mask:0xf bank_mask:0xf bound_ctrl:1
	v_mov_b32_e32 v106, v89
	s_nop 1
	v_permlane16_swap_b32_e32 v89, v106
	v_max_u32_e32 v89, v89, v106
	v_mov_b32_e32 v106, v89
	s_nop 1
	v_permlane32_swap_b32_e32 v89, v106
	v_max_u32_e32 v89, v89, v106
	s_nop 0
	v_readfirstlane_b32 s0, v89
	s_and_b32 s7, s0, 0xff800000
	s_lshr_b32 s0, s0, 23
	s_min_u32 s0, s0, 3
	s_mov_b32 s21, 0
	s_add_i32 s5, s0, 1
	s_branch .LBB0_1100

.LBB0_1100:
	v_mov_b32_e32 v106, v199
	v_mov_b32_e32 v107, v199
	s_mov_b32 s4, s7
	v_mov_b32_e32 v89, s7
	v_cmp_ge_u32_e64 s[0:1], v62, v89
	v_cmp_ge_u32_e64 s[2:3], v63, v89
	v_cmp_ge_u32_e64 s[6:7], v60, v89
	v_cmp_ge_u32_e64 s[8:9], v61, v89
	v_cmp_ge_u32_e64 s[10:11], v58, v89
	v_cmp_ge_u32_e64 s[12:13], v59, v89
	v_cmp_ge_u32_e64 s[14:15], v56, v89
	v_cmp_ge_u32_e64 s[16:17], v57, v89
	v_addc_co_u32_e64 v106, s[0:1], v106, 0, s[0:1]
	v_addc_co_u32_e64 v107, s[2:3], v107, 0, s[2:3]
	v_addc_co_u32_e64 v106, s[6:7], v106, 0, s[6:7]
	v_addc_co_u32_e64 v107, s[8:9], v107, 0, s[8:9]
	v_addc_co_u32_e64 v106, s[10:11], v106, 0, s[10:11]
	v_addc_co_u32_e64 v107, s[12:13], v107, 0, s[12:13]
	v_addc_co_u32_e64 v106, s[14:15], v106, 0, s[14:15]
	v_addc_co_u32_e64 v107, s[16:17], v107, 0, s[16:17]
	s_nop 0
	v_cmp_ge_u32_e64 s[0:1], v104, v89
	v_cmp_ge_u32_e64 s[2:3], v105, v89
	v_cmp_ge_u32_e64 s[6:7], v102, v89
	v_cmp_ge_u32_e64 s[8:9], v103, v89
	v_cmp_ge_u32_e64 s[10:11], v100, v89
	v_cmp_ge_u32_e64 s[12:13], v101, v89
	v_cmp_ge_u32_e64 s[14:15], v98, v89
	v_cmp_ge_u32_e64 s[16:17], v99, v89
	v_addc_co_u32_e64 v106, s[0:1], v106, 0, s[0:1]
	v_addc_co_u32_e64 v107, s[2:3], v107, 0, s[2:3]
	v_addc_co_u32_e64 v106, s[6:7], v106, 0, s[6:7]
	v_addc_co_u32_e64 v107, s[8:9], v107, 0, s[8:9]
	v_addc_co_u32_e64 v106, s[10:11], v106, 0, s[10:11]
	v_addc_co_u32_e64 v107, s[12:13], v107, 0, s[12:13]
	v_addc_co_u32_e64 v106, s[14:15], v106, 0, s[14:15]
	v_addc_co_u32_e64 v107, s[16:17], v107, 0, s[16:17]
	s_nop 0
	v_cmp_ge_u32_e64 s[0:1], v96, v89
	v_cmp_ge_u32_e64 s[2:3], v97, v89
	v_cmp_ge_u32_e64 s[6:7], v94, v89
	v_cmp_ge_u32_e64 s[8:9], v95, v89
	v_cmp_ge_u32_e64 s[10:11], v92, v89
	v_cmp_ge_u32_e64 s[12:13], v93, v89
	v_cmp_ge_u32_e64 s[14:15], v90, v89
	v_cmp_ge_u32_e64 s[16:17], v91, v89
	v_addc_co_u32_e64 v106, s[0:1], v106, 0, s[0:1]
	v_addc_co_u32_e64 v107, s[2:3], v107, 0, s[2:3]
	v_addc_co_u32_e64 v106, s[6:7], v106, 0, s[6:7]
	v_addc_co_u32_e64 v107, s[8:9], v107, 0, s[8:9]
	v_addc_co_u32_e64 v106, s[10:11], v106, 0, s[10:11]
	v_addc_co_u32_e64 v107, s[12:13], v107, 0, s[12:13]
	v_addc_co_u32_e64 v106, s[14:15], v106, 0, s[14:15]
	v_addc_co_u32_e64 v107, s[16:17], v107, 0, s[16:17]
	s_nop 0
	v_cmp_ge_u32_e64 s[0:1], v86, v89
	v_cmp_ge_u32_e64 s[2:3], v87, v89
	v_cmp_ge_u32_e64 s[6:7], v84, v89
	v_cmp_ge_u32_e64 s[8:9], v85, v89
	v_cmp_ge_u32_e64 s[10:11], v82, v89
	v_cmp_ge_u32_e64 s[12:13], v83, v89
	v_cmp_ge_u32_e64 s[14:15], v80, v89
	v_cmp_ge_u32_e64 s[16:17], v81, v89
	v_addc_co_u32_e64 v106, s[0:1], v106, 0, s[0:1]
	v_addc_co_u32_e64 v107, s[2:3], v107, 0, s[2:3]
	v_addc_co_u32_e64 v106, s[6:7], v106, 0, s[6:7]
	v_addc_co_u32_e64 v107, s[8:9], v107, 0, s[8:9]
	v_addc_co_u32_e64 v106, s[10:11], v106, 0, s[10:11]
	v_addc_co_u32_e64 v107, s[12:13], v107, 0, s[12:13]
	v_addc_co_u32_e64 v106, s[14:15], v106, 0, s[14:15]
	v_addc_co_u32_e64 v107, s[16:17], v107, 0, s[16:17]
	s_nop 0
	v_cmp_ge_u32_e64 s[0:1], v78, v89
	v_cmp_ge_u32_e64 s[2:3], v79, v89
	v_cmp_ge_u32_e64 s[6:7], v76, v89
	v_cmp_ge_u32_e64 s[8:9], v77, v89
	v_cmp_ge_u32_e64 s[10:11], v74, v89
	v_cmp_ge_u32_e64 s[12:13], v75, v89
	v_cmp_ge_u32_e64 s[14:15], v72, v89
	v_cmp_ge_u32_e64 s[16:17], v73, v89
	v_addc_co_u32_e64 v106, s[0:1], v106, 0, s[0:1]
	v_addc_co_u32_e64 v107, s[2:3], v107, 0, s[2:3]
	v_addc_co_u32_e64 v106, s[6:7], v106, 0, s[6:7]
	v_addc_co_u32_e64 v107, s[8:9], v107, 0, s[8:9]
	v_addc_co_u32_e64 v106, s[10:11], v106, 0, s[10:11]
	v_addc_co_u32_e64 v107, s[12:13], v107, 0, s[12:13]
	v_addc_co_u32_e64 v106, s[14:15], v106, 0, s[14:15]
	v_addc_co_u32_e64 v107, s[16:17], v107, 0, s[16:17]
	s_nop 0
	v_cmp_ge_u32_e64 s[0:1], v70, v89
	v_cmp_ge_u32_e64 s[2:3], v71, v89
	v_cmp_ge_u32_e64 s[6:7], v68, v89
	v_cmp_ge_u32_e64 s[8:9], v69, v89
	v_cmp_ge_u32_e64 s[10:11], v66, v89
	v_cmp_ge_u32_e64 s[12:13], v67, v89
	v_cmp_ge_u32_e64 s[14:15], v64, v89
	v_cmp_ge_u32_e64 s[16:17], v65, v89
	v_addc_co_u32_e64 v106, s[0:1], v106, 0, s[0:1]
	v_addc_co_u32_e64 v107, s[2:3], v107, 0, s[2:3]
	v_addc_co_u32_e64 v106, s[6:7], v106, 0, s[6:7]
	v_addc_co_u32_e64 v107, s[8:9], v107, 0, s[8:9]
	v_addc_co_u32_e64 v106, s[10:11], v106, 0, s[10:11]
	v_addc_co_u32_e64 v107, s[12:13], v107, 0, s[12:13]
	v_addc_co_u32_e64 v106, s[14:15], v106, 0, s[14:15]
	v_addc_co_u32_e64 v107, s[16:17], v107, 0, s[16:17]
	s_mov_b64 s[0:1], -1
	v_add_u32_e32 v89, v106, v107
	s_mov_b64 s[2:3], -1
	s_nop 0
	v_add_u32_dpp v89, v89, v89 quad_perm:[1,0,3,2] row_mask:0xf bank_mask:0xf bound_ctrl:1
	s_nop 1
	v_add_u32_dpp v89, v89, v89 quad_perm:[2,3,0,1] row_mask:0xf bank_mask:0xf bound_ctrl:1
	s_nop 1
	v_add_u32_dpp v89, v89, v89 row_half_mirror row_mask:0xf bank_mask:0xf bound_ctrl:1
	s_nop 1
	v_add_u32_dpp v89, v89, v89 row_mirror row_mask:0xf bank_mask:0xf bound_ctrl:1
	v_mov_b32_e32 v106, v89
	s_nop 1
	v_permlane16_swap_b32_e32 v89, v106
	v_add_u32_e32 v89, v89, v106
	v_mov_b32_e32 v106, v89
	s_nop 1
	v_permlane32_swap_b32_e32 v89, v106
	v_add_u32_e32 v89, v89, v106
	s_nop 0
	v_readfirstlane_b32 s6, v89
	s_cmpk_lt_i32 s6, 0x100
	s_cbranch_scc0 .LBB0_1099
	s_mov_b32 s21, s6
	s_add_i32 s5, s5, -1
	s_add_i32 s7, s4, 0xff800000
	s_cmp_eq_u32 s5, 0
	s_mov_b64 s[0:1], 0
	s_cselect_b64 s[2:3], -1, 0
	s_branch .LBB0_1099

.Lsf1106_loop:
	s_sub_i32 s25, s22, s20
	s_cmp_lt_u32 s25, 2
	s_cbranch_scc1 .Lsf1106_tie
	s_sub_i32 s26, s23, s21
	s_sub_i32 s27, s23, 0x100
	v_cvt_f32_u32_e32 v108, s25
	v_cvt_f32_u32_e32 v109, s26
	v_cvt_f32_u32_e32 v107, s27
	v_rcp_f32_e32 v109, v109
	v_add_f32_e32 v107, 0.5, v107
	s_nop 0
	v_mul_f32_e32 v108, v108, v109
	v_mul_f32_e32 v107, v107, v108
	v_cvt_u32_f32_e32 v107, v107
	s_nop 0
	v_readfirstlane_b32 s27, v107
	s_sub_i32 s28, s25, 1
	s_max_u32 s27, s27, 1
	s_min_u32 s27, s27, s28
	s_add_i32 s27, s20, s27
	v_mov_b32_e32 v107, s27
	v_mov_b32_e32 v108, v199
	v_mov_b32_e32 v109, v199
	v_cmp_ge_u32_e64 s[2:3], v62, v107
	v_cmp_ge_u32_e64 s[4:5], v63, v107
	v_cmp_ge_u32_e64 s[6:7], v60, v107
	v_cmp_ge_u32_e64 s[8:9], v61, v107
	v_cmp_ge_u32_e64 s[10:11], v58, v107
	v_cmp_ge_u32_e64 s[12:13], v59, v107
	v_cmp_ge_u32_e64 s[14:15], v56, v107
	v_cmp_ge_u32_e64 s[16:17], v57, v107
	v_addc_co_u32_e64 v108, s[2:3], v108, 0, s[2:3]
	v_addc_co_u32_e64 v109, s[4:5], v109, 0, s[4:5]
	v_addc_co_u32_e64 v108, s[6:7], v108, 0, s[6:7]
	v_addc_co_u32_e64 v109, s[8:9], v109, 0, s[8:9]
	v_addc_co_u32_e64 v108, s[10:11], v108, 0, s[10:11]
	v_addc_co_u32_e64 v109, s[12:13], v109, 0, s[12:13]
	v_addc_co_u32_e64 v108, s[14:15], v108, 0, s[14:15]
	v_addc_co_u32_e64 v109, s[16:17], v109, 0, s[16:17]
	s_nop 0
	v_cmp_ge_u32_e64 s[2:3], v104, v107
	v_cmp_ge_u32_e64 s[4:5], v105, v107
	v_cmp_ge_u32_e64 s[6:7], v102, v107
	v_cmp_ge_u32_e64 s[8:9], v103, v107
	v_cmp_ge_u32_e64 s[10:11], v100, v107
	v_cmp_ge_u32_e64 s[12:13], v101, v107
	v_cmp_ge_u32_e64 s[14:15], v98, v107
	v_cmp_ge_u32_e64 s[16:17], v99, v107
	v_addc_co_u32_e64 v108, s[2:3], v108, 0, s[2:3]
	v_addc_co_u32_e64 v109, s[4:5], v109, 0, s[4:5]
	v_addc_co_u32_e64 v108, s[6:7], v108, 0, s[6:7]
	v_addc_co_u32_e64 v109, s[8:9], v109, 0, s[8:9]
	v_addc_co_u32_e64 v108, s[10:11], v108, 0, s[10:11]
	v_addc_co_u32_e64 v109, s[12:13], v109, 0, s[12:13]
	v_addc_co_u32_e64 v108, s[14:15], v108, 0, s[14:15]
	v_addc_co_u32_e64 v109, s[16:17], v109, 0, s[16:17]
	s_nop 0
	v_cmp_ge_u32_e64 s[2:3], v96, v107
	v_cmp_ge_u32_e64 s[4:5], v97, v107
	v_cmp_ge_u32_e64 s[6:7], v94, v107
	v_cmp_ge_u32_e64 s[8:9], v95, v107
	v_cmp_ge_u32_e64 s[10:11], v92, v107
	v_cmp_ge_u32_e64 s[12:13], v93, v107
	v_cmp_ge_u32_e64 s[14:15], v90, v107
	v_cmp_ge_u32_e64 s[16:17], v91, v107
	v_addc_co_u32_e64 v108, s[2:3], v108, 0, s[2:3]
	v_addc_co_u32_e64 v109, s[4:5], v109, 0, s[4:5]
	v_addc_co_u32_e64 v108, s[6:7], v108, 0, s[6:7]
	v_addc_co_u32_e64 v109, s[8:9], v109, 0, s[8:9]
	v_addc_co_u32_e64 v108, s[10:11], v108, 0, s[10:11]
	v_addc_co_u32_e64 v109, s[12:13], v109, 0, s[12:13]
	v_addc_co_u32_e64 v108, s[14:15], v108, 0, s[14:15]
	v_addc_co_u32_e64 v109, s[16:17], v109, 0, s[16:17]
	s_nop 0
	v_cmp_ge_u32_e64 s[2:3], v86, v107
	v_cmp_ge_u32_e64 s[4:5], v87, v107
	v_cmp_ge_u32_e64 s[6:7], v84, v107
	v_cmp_ge_u32_e64 s[8:9], v85, v107
	v_cmp_ge_u32_e64 s[10:11], v82, v107
	v_cmp_ge_u32_e64 s[12:13], v83, v107
	v_cmp_ge_u32_e64 s[14:15], v80, v107
	v_cmp_ge_u32_e64 s[16:17], v81, v107
	v_addc_co_u32_e64 v108, s[2:3], v108, 0, s[2:3]
	v_addc_co_u32_e64 v109, s[4:5], v109, 0, s[4:5]
	v_addc_co_u32_e64 v108, s[6:7], v108, 0, s[6:7]
	v_addc_co_u32_e64 v109, s[8:9], v109, 0, s[8:9]
	v_addc_co_u32_e64 v108, s[10:11], v108, 0, s[10:11]
	v_addc_co_u32_e64 v109, s[12:13], v109, 0, s[12:13]
	v_addc_co_u32_e64 v108, s[14:15], v108, 0, s[14:15]
	v_addc_co_u32_e64 v109, s[16:17], v109, 0, s[16:17]
	s_nop 0
	v_cmp_ge_u32_e64 s[2:3], v78, v107
	v_cmp_ge_u32_e64 s[4:5], v79, v107
	v_cmp_ge_u32_e64 s[6:7], v76, v107
	v_cmp_ge_u32_e64 s[8:9], v77, v107
	v_cmp_ge_u32_e64 s[10:11], v74, v107
	v_cmp_ge_u32_e64 s[12:13], v75, v107
	v_cmp_ge_u32_e64 s[14:15], v72, v107
	v_cmp_ge_u32_e64 s[16:17], v73, v107
	v_addc_co_u32_e64 v108, s[2:3], v108, 0, s[2:3]
	v_addc_co_u32_e64 v109, s[4:5], v109, 0, s[4:5]
	v_addc_co_u32_e64 v108, s[6:7], v108, 0, s[6:7]
	v_addc_co_u32_e64 v109, s[8:9], v109, 0, s[8:9]
	v_addc_co_u32_e64 v108, s[10:11], v108, 0, s[10:11]
	v_addc_co_u32_e64 v109, s[12:13], v109, 0, s[12:13]
	v_addc_co_u32_e64 v108, s[14:15], v108, 0, s[14:15]
	v_addc_co_u32_e64 v109, s[16:17], v109, 0, s[16:17]
	s_nop 0
	v_cmp_ge_u32_e64 s[2:3], v70, v107
	v_cmp_ge_u32_e64 s[4:5], v71, v107
	v_cmp_ge_u32_e64 s[6:7], v68, v107
	v_cmp_ge_u32_e64 s[8:9], v69, v107
	v_cmp_ge_u32_e64 s[10:11], v66, v107
	v_cmp_ge_u32_e64 s[12:13], v67, v107
	v_cmp_ge_u32_e64 s[14:15], v64, v107
	v_cmp_ge_u32_e64 s[16:17], v65, v107
	v_addc_co_u32_e64 v108, s[2:3], v108, 0, s[2:3]
	v_addc_co_u32_e64 v109, s[4:5], v109, 0, s[4:5]
	v_addc_co_u32_e64 v108, s[6:7], v108, 0, s[6:7]
	v_addc_co_u32_e64 v109, s[8:9], v109, 0, s[8:9]
	v_addc_co_u32_e64 v108, s[10:11], v108, 0, s[10:11]
	v_addc_co_u32_e64 v109, s[12:13], v109, 0, s[12:13]
	v_addc_co_u32_e64 v108, s[14:15], v108, 0, s[14:15]
	v_addc_co_u32_e64 v109, s[16:17], v109, 0, s[16:17]
	s_nop 0
	v_add_u32_e32 v108, v108, v109
	s_nop 1
	v_add_u32_dpp v108, v108, v108 quad_perm:[1,0,3,2] row_mask:0xf bank_mask:0xf bound_ctrl:1
	s_nop 1
	v_add_u32_dpp v108, v108, v108 quad_perm:[2,3,0,1] row_mask:0xf bank_mask:0xf bound_ctrl:1
	s_nop 1
	v_add_u32_dpp v108, v108, v108 row_half_mirror row_mask:0xf bank_mask:0xf bound_ctrl:1
	s_nop 1
	v_add_u32_dpp v108, v108, v108 row_mirror row_mask:0xf bank_mask:0xf bound_ctrl:1
	v_mov_b32_e32 v109, v108
	s_nop 1
	v_permlane16_swap_b32_e32 v108, v109
	v_add_u32_e32 v108, v108, v109
	v_mov_b32_e32 v109, v108
	s_nop 1
	v_permlane32_swap_b32_e32 v108, v109
	v_add_u32_e32 v108, v108, v109
	s_nop 0
	v_readfirstlane_b32 s29, v108
	s_cmpk_eq_i32 s29, 0x100
	s_cbranch_scc1 .Lsf1106_hit
	s_cmpk_gt_i32 s29, 0x100
	s_cbranch_scc1 .Lsf1106_up
	s_mov_b32 s22, s27
	s_mov_b32 s21, s29
	s_cmp_eq_u32 s31, 2
	s_cbranch_scc0 .Lsf1106_hd
	s_sub_i32 s26, s23, 0x100
	s_lshr_b32 s26, s26, 1
	s_max_u32 s26, s26, 1
	s_add_i32 s23, s26, 0x100

.LBB0_1400:
	v_readlane_b32 s0, v254, 52
	s_cmp_gt_i32 s0, 4
	s_mov_b64 s[0:1], -1
	s_cbranch_scc0 .LBB0_1655
	s_waitcnt lgkmcnt(3)
	v_max_u32_e32 v89, v63, v62
	s_waitcnt lgkmcnt(2)
	v_max3_u32 v89, v61, v60, v89
	s_waitcnt lgkmcnt(1)
	v_max3_u32 v89, v59, v58, v89
	s_waitcnt lgkmcnt(0)
	v_max3_u32 v89, v57, v56, v89
	ds_read2st64_b32 v[96:97], v183 offset0:8 offset1:9
	ds_read2st64_b32 v[94:95], v183 offset0:10 offset1:11
	ds_read2st64_b32 v[92:93], v183 offset0:12 offset1:13
	ds_read2st64_b32 v[90:91], v183 offset0:14 offset1:15
	ds_read2st64_b32 v[86:87], v183 offset0:16 offset1:17
	ds_read2st64_b32 v[84:85], v183 offset0:18 offset1:19
	ds_read2st64_b32 v[82:83], v183 offset0:20 offset1:21
	ds_read2st64_b32 v[80:81], v183 offset0:22 offset1:23
	ds_read2st64_b32 v[78:79], v183 offset0:24 offset1:25
	ds_read2st64_b32 v[76:77], v183 offset0:26 offset1:27
	ds_read2st64_b32 v[74:75], v183 offset0:28 offset1:29
	ds_read2st64_b32 v[72:73], v183 offset0:30 offset1:31
	ds_read2st64_b32 v[70:71], v183 offset0:32 offset1:33
	ds_read2st64_b32 v[68:69], v183 offset0:34 offset1:35
	ds_read2st64_b32 v[66:67], v183 offset0:36 offset1:37
	ds_read2st64_b32 v[64:65], v183 offset0:38 offset1:39
	s_waitcnt lgkmcnt(14)
	v_max3_u32 v89, v97, v96, v89
	v_max3_u32 v89, v95, v94, v89
	s_waitcnt lgkmcnt(13)
	v_max3_u32 v89, v93, v92, v89
	s_waitcnt lgkmcnt(12)
	v_max3_u32 v89, v91, v90, v89
	s_waitcnt lgkmcnt(11)
	v_max3_u32 v89, v87, v86, v89
	s_waitcnt lgkmcnt(10)
	v_max3_u32 v89, v85, v84, v89
	s_waitcnt lgkmcnt(9)
	v_max3_u32 v89, v83, v82, v89
	s_waitcnt lgkmcnt(8)
	v_max3_u32 v89, v81, v80, v89
	s_waitcnt lgkmcnt(7)
	v_max3_u32 v89, v79, v78, v89
	s_waitcnt lgkmcnt(6)
	v_max3_u32 v89, v77, v76, v89
	s_waitcnt lgkmcnt(5)
	v_max3_u32 v89, v75, v74, v89
	s_waitcnt lgkmcnt(4)
	v_max3_u32 v89, v73, v72, v89
	s_waitcnt lgkmcnt(3)
	v_max3_u32 v89, v71, v70, v89
	s_waitcnt lgkmcnt(2)
	v_max3_u32 v89, v69, v68, v89
	s_waitcnt lgkmcnt(1)
	v_max3_u32 v89, v67, v66, v89
	s_waitcnt lgkmcnt(0)
	v_max3_u32 v89, v65, v64, v89
	s_nop 1
	v_max_u32_dpp v89, v89, v89 quad_perm:[1,0,3,2] row_mask:0xf bank_mask:0xf bound_ctrl:1
	s_nop 1
	v_max_u32_dpp v89, v89, v89 quad_perm:[2,3,0,1] row_mask:0xf bank_mask:0xf bound_ctrl:1
	s_nop 1
	v_max_u32_dpp v89, v89, v89 row_half_mirror row_mask:0xf bank_mask:0xf bound_ctrl:1
	s_nop 1
	v_max_u32_dpp v89, v89, v89 row_mirror row_mask:0xf bank_mask:0xf bound_ctrl:1
	v_mov_b32_e32 v98, v89
	s_nop 1
	v_permlane16_swap_b32_e32 v89, v98
	v_max_u32_e32 v89, v89, v98
	v_mov_b32_e32 v98, v89
	s_nop 1
	v_permlane32_swap_b32_e32 v89, v98
	v_max_u32_e32 v89, v89, v98
	s_nop 0
	v_readfirstlane_b32 s0, v89
	s_and_b32 s7, s0, 0xff800000
	s_lshr_b32 s0, s0, 23
	s_min_u32 s0, s0, 3
	s_mov_b32 s21, 0
	s_add_i32 s5, s0, 1
	s_branch .LBB0_1403

.LBB0_1403:
	v_mov_b32_e32 v98, v199
	v_mov_b32_e32 v99, v199
	s_mov_b32 s4, s7
	v_mov_b32_e32 v89, s7
	v_cmp_ge_u32_e64 s[0:1], v62, v89
	v_cmp_ge_u32_e64 s[2:3], v63, v89
	v_cmp_ge_u32_e64 s[6:7], v60, v89
	v_cmp_ge_u32_e64 s[8:9], v61, v89
	v_cmp_ge_u32_e64 s[10:11], v58, v89
	v_cmp_ge_u32_e64 s[12:13], v59, v89
	v_cmp_ge_u32_e64 s[14:15], v56, v89
	v_cmp_ge_u32_e64 s[16:17], v57, v89
	v_addc_co_u32_e64 v98, s[0:1], v98, 0, s[0:1]
	v_addc_co_u32_e64 v99, s[2:3], v99, 0, s[2:3]
	v_addc_co_u32_e64 v98, s[6:7], v98, 0, s[6:7]
	v_addc_co_u32_e64 v99, s[8:9], v99, 0, s[8:9]
	v_addc_co_u32_e64 v98, s[10:11], v98, 0, s[10:11]
	v_addc_co_u32_e64 v99, s[12:13], v99, 0, s[12:13]
	v_addc_co_u32_e64 v98, s[14:15], v98, 0, s[14:15]
	v_addc_co_u32_e64 v99, s[16:17], v99, 0, s[16:17]
	s_nop 0
	v_cmp_ge_u32_e64 s[0:1], v96, v89
	v_cmp_ge_u32_e64 s[2:3], v97, v89
	v_cmp_ge_u32_e64 s[6:7], v94, v89
	v_cmp_ge_u32_e64 s[8:9], v95, v89
	v_cmp_ge_u32_e64 s[10:11], v92, v89
	v_cmp_ge_u32_e64 s[12:13], v93, v89
	v_cmp_ge_u32_e64 s[14:15], v90, v89
	v_cmp_ge_u32_e64 s[16:17], v91, v89
	v_addc_co_u32_e64 v98, s[0:1], v98, 0, s[0:1]
	v_addc_co_u32_e64 v99, s[2:3], v99, 0, s[2:3]
	v_addc_co_u32_e64 v98, s[6:7], v98, 0, s[6:7]
	v_addc_co_u32_e64 v99, s[8:9], v99, 0, s[8:9]
	v_addc_co_u32_e64 v98, s[10:11], v98, 0, s[10:11]
	v_addc_co_u32_e64 v99, s[12:13], v99, 0, s[12:13]
	v_addc_co_u32_e64 v98, s[14:15], v98, 0, s[14:15]
	v_addc_co_u32_e64 v99, s[16:17], v99, 0, s[16:17]
	s_nop 0
	v_cmp_ge_u32_e64 s[0:1], v86, v89
	v_cmp_ge_u32_e64 s[2:3], v87, v89
	v_cmp_ge_u32_e64 s[6:7], v84, v89
	v_cmp_ge_u32_e64 s[8:9], v85, v89
	v_cmp_ge_u32_e64 s[10:11], v82, v89
	v_cmp_ge_u32_e64 s[12:13], v83, v89
	v_cmp_ge_u32_e64 s[14:15], v80, v89
	v_cmp_ge_u32_e64 s[16:17], v81, v89
	v_addc_co_u32_e64 v98, s[0:1], v98, 0, s[0:1]
	v_addc_co_u32_e64 v99, s[2:3], v99, 0, s[2:3]
	v_addc_co_u32_e64 v98, s[6:7], v98, 0, s[6:7]
	v_addc_co_u32_e64 v99, s[8:9], v99, 0, s[8:9]
	v_addc_co_u32_e64 v98, s[10:11], v98, 0, s[10:11]
	v_addc_co_u32_e64 v99, s[12:13], v99, 0, s[12:13]
	v_addc_co_u32_e64 v98, s[14:15], v98, 0, s[14:15]
	v_addc_co_u32_e64 v99, s[16:17], v99, 0, s[16:17]
	s_nop 0
	v_cmp_ge_u32_e64 s[0:1], v78, v89
	v_cmp_ge_u32_e64 s[2:3], v79, v89
	v_cmp_ge_u32_e64 s[6:7], v76, v89
	v_cmp_ge_u32_e64 s[8:9], v77, v89
	v_cmp_ge_u32_e64 s[10:11], v74, v89
	v_cmp_ge_u32_e64 s[12:13], v75, v89
	v_cmp_ge_u32_e64 s[14:15], v72, v89
	v_cmp_ge_u32_e64 s[16:17], v73, v89
	v_addc_co_u32_e64 v98, s[0:1], v98, 0, s[0:1]
	v_addc_co_u32_e64 v99, s[2:3], v99, 0, s[2:3]
	v_addc_co_u32_e64 v98, s[6:7], v98, 0, s[6:7]
	v_addc_co_u32_e64 v99, s[8:9], v99, 0, s[8:9]
	v_addc_co_u32_e64 v98, s[10:11], v98, 0, s[10:11]
	v_addc_co_u32_e64 v99, s[12:13], v99, 0, s[12:13]
	v_addc_co_u32_e64 v98, s[14:15], v98, 0, s[14:15]
	v_addc_co_u32_e64 v99, s[16:17], v99, 0, s[16:17]
	s_nop 0
	v_cmp_ge_u32_e64 s[0:1], v70, v89
	v_cmp_ge_u32_e64 s[2:3], v71, v89
	v_cmp_ge_u32_e64 s[6:7], v68, v89
	v_cmp_ge_u32_e64 s[8:9], v69, v89
	v_cmp_ge_u32_e64 s[10:11], v66, v89
	v_cmp_ge_u32_e64 s[12:13], v67, v89
	v_cmp_ge_u32_e64 s[14:15], v64, v89
	v_cmp_ge_u32_e64 s[16:17], v65, v89
	v_addc_co_u32_e64 v98, s[0:1], v98, 0, s[0:1]
	v_addc_co_u32_e64 v99, s[2:3], v99, 0, s[2:3]
	v_addc_co_u32_e64 v98, s[6:7], v98, 0, s[6:7]
	v_addc_co_u32_e64 v99, s[8:9], v99, 0, s[8:9]
	v_addc_co_u32_e64 v98, s[10:11], v98, 0, s[10:11]
	v_addc_co_u32_e64 v99, s[12:13], v99, 0, s[12:13]
	v_addc_co_u32_e64 v98, s[14:15], v98, 0, s[14:15]
	v_addc_co_u32_e64 v99, s[16:17], v99, 0, s[16:17]
	s_mov_b64 s[0:1], -1
	v_add_u32_e32 v89, v98, v99
	s_mov_b64 s[2:3], -1
	s_nop 0
	v_add_u32_dpp v89, v89, v89 quad_perm:[1,0,3,2] row_mask:0xf bank_mask:0xf bound_ctrl:1
	s_nop 1
	v_add_u32_dpp v89, v89, v89 quad_perm:[2,3,0,1] row_mask:0xf bank_mask:0xf bound_ctrl:1
	s_nop 1
	v_add_u32_dpp v89, v89, v89 row_half_mirror row_mask:0xf bank_mask:0xf bound_ctrl:1
	s_nop 1
	v_add_u32_dpp v89, v89, v89 row_mirror row_mask:0xf bank_mask:0xf bound_ctrl:1
	v_mov_b32_e32 v98, v89
	s_nop 1
	v_permlane16_swap_b32_e32 v89, v98
	v_add_u32_e32 v89, v89, v98
	v_mov_b32_e32 v98, v89
	s_nop 1
	v_permlane32_swap_b32_e32 v89, v98
	v_add_u32_e32 v89, v89, v98
	s_nop 0
	v_readfirstlane_b32 s6, v89
	s_cmpk_lt_i32 s6, 0x100
	s_cbranch_scc0 .LBB0_1402
	s_mov_b32 s21, s6
	s_add_i32 s5, s5, -1
	s_add_i32 s7, s4, 0xff800000
	s_cmp_eq_u32 s5, 0
	s_mov_b64 s[0:1], 0
	s_cselect_b64 s[2:3], -1, 0
	s_branch .LBB0_1402

.Lsf1409_loop:
	s_sub_i32 s25, s22, s20
	s_cmp_lt_u32 s25, 2
	s_cbranch_scc1 .Lsf1409_tie
	s_sub_i32 s26, s23, s21
	s_sub_i32 s27, s23, 0x100
	v_cvt_f32_u32_e32 v100, s25
	v_cvt_f32_u32_e32 v101, s26
	v_cvt_f32_u32_e32 v99, s27
	v_rcp_f32_e32 v101, v101
	v_add_f32_e32 v99, 0.5, v99
	s_nop 0
	v_mul_f32_e32 v100, v100, v101
	v_mul_f32_e32 v99, v99, v100
	v_cvt_u32_f32_e32 v99, v99
	s_nop 0
	v_readfirstlane_b32 s27, v99
	s_sub_i32 s28, s25, 1
	s_max_u32 s27, s27, 1
	s_min_u32 s27, s27, s28
	s_add_i32 s27, s20, s27
	v_mov_b32_e32 v99, s27
	v_mov_b32_e32 v100, v199
	v_mov_b32_e32 v101, v199
	v_cmp_ge_u32_e64 s[2:3], v62, v99
	v_cmp_ge_u32_e64 s[4:5], v63, v99
	v_cmp_ge_u32_e64 s[6:7], v60, v99
	v_cmp_ge_u32_e64 s[8:9], v61, v99
	v_cmp_ge_u32_e64 s[10:11], v58, v99
	v_cmp_ge_u32_e64 s[12:13], v59, v99
	v_cmp_ge_u32_e64 s[14:15], v56, v99
	v_cmp_ge_u32_e64 s[16:17], v57, v99
	v_addc_co_u32_e64 v100, s[2:3], v100, 0, s[2:3]
	v_addc_co_u32_e64 v101, s[4:5], v101, 0, s[4:5]
	v_addc_co_u32_e64 v100, s[6:7], v100, 0, s[6:7]
	v_addc_co_u32_e64 v101, s[8:9], v101, 0, s[8:9]
	v_addc_co_u32_e64 v100, s[10:11], v100, 0, s[10:11]
	v_addc_co_u32_e64 v101, s[12:13], v101, 0, s[12:13]
	v_addc_co_u32_e64 v100, s[14:15], v100, 0, s[14:15]
	v_addc_co_u32_e64 v101, s[16:17], v101, 0, s[16:17]
	s_nop 0
	v_cmp_ge_u32_e64 s[2:3], v96, v99
	v_cmp_ge_u32_e64 s[4:5], v97, v99
	v_cmp_ge_u32_e64 s[6:7], v94, v99
	v_cmp_ge_u32_e64 s[8:9], v95, v99
	v_cmp_ge_u32_e64 s[10:11], v92, v99
	v_cmp_ge_u32_e64 s[12:13], v93, v99
	v_cmp_ge_u32_e64 s[14:15], v90, v99
	v_cmp_ge_u32_e64 s[16:17], v91, v99
	v_addc_co_u32_e64 v100, s[2:3], v100, 0, s[2:3]
	v_addc_co_u32_e64 v101, s[4:5], v101, 0, s[4:5]
	v_addc_co_u32_e64 v100, s[6:7], v100, 0, s[6:7]
	v_addc_co_u32_e64 v101, s[8:9], v101, 0, s[8:9]
	v_addc_co_u32_e64 v100, s[10:11], v100, 0, s[10:11]
	v_addc_co_u32_e64 v101, s[12:13], v101, 0, s[12:13]
	v_addc_co_u32_e64 v100, s[14:15], v100, 0, s[14:15]
	v_addc_co_u32_e64 v101, s[16:17], v101, 0, s[16:17]
	s_nop 0
	v_cmp_ge_u32_e64 s[2:3], v86, v99
	v_cmp_ge_u32_e64 s[4:5], v87, v99
	v_cmp_ge_u32_e64 s[6:7], v84, v99
	v_cmp_ge_u32_e64 s[8:9], v85, v99
	v_cmp_ge_u32_e64 s[10:11], v82, v99
	v_cmp_ge_u32_e64 s[12:13], v83, v99
	v_cmp_ge_u32_e64 s[14:15], v80, v99
	v_cmp_ge_u32_e64 s[16:17], v81, v99
	v_addc_co_u32_e64 v100, s[2:3], v100, 0, s[2:3]
	v_addc_co_u32_e64 v101, s[4:5], v101, 0, s[4:5]
	v_addc_co_u32_e64 v100, s[6:7], v100, 0, s[6:7]
	v_addc_co_u32_e64 v101, s[8:9], v101, 0, s[8:9]
	v_addc_co_u32_e64 v100, s[10:11], v100, 0, s[10:11]
	v_addc_co_u32_e64 v101, s[12:13], v101, 0, s[12:13]
	v_addc_co_u32_e64 v100, s[14:15], v100, 0, s[14:15]
	v_addc_co_u32_e64 v101, s[16:17], v101, 0, s[16:17]
	s_nop 0
	v_cmp_ge_u32_e64 s[2:3], v78, v99
	v_cmp_ge_u32_e64 s[4:5], v79, v99
	v_cmp_ge_u32_e64 s[6:7], v76, v99
	v_cmp_ge_u32_e64 s[8:9], v77, v99
	v_cmp_ge_u32_e64 s[10:11], v74, v99
	v_cmp_ge_u32_e64 s[12:13], v75, v99
	v_cmp_ge_u32_e64 s[14:15], v72, v99
	v_cmp_ge_u32_e64 s[16:17], v73, v99
	v_addc_co_u32_e64 v100, s[2:3], v100, 0, s[2:3]
	v_addc_co_u32_e64 v101, s[4:5], v101, 0, s[4:5]
	v_addc_co_u32_e64 v100, s[6:7], v100, 0, s[6:7]
	v_addc_co_u32_e64 v101, s[8:9], v101, 0, s[8:9]
	v_addc_co_u32_e64 v100, s[10:11], v100, 0, s[10:11]
	v_addc_co_u32_e64 v101, s[12:13], v101, 0, s[12:13]
	v_addc_co_u32_e64 v100, s[14:15], v100, 0, s[14:15]
	v_addc_co_u32_e64 v101, s[16:17], v101, 0, s[16:17]
	s_nop 0
	v_cmp_ge_u32_e64 s[2:3], v70, v99
	v_cmp_ge_u32_e64 s[4:5], v71, v99
	v_cmp_ge_u32_e64 s[6:7], v68, v99
	v_cmp_ge_u32_e64 s[8:9], v69, v99
	v_cmp_ge_u32_e64 s[10:11], v66, v99
	v_cmp_ge_u32_e64 s[12:13], v67, v99
	v_cmp_ge_u32_e64 s[14:15], v64, v99
	v_cmp_ge_u32_e64 s[16:17], v65, v99
	v_addc_co_u32_e64 v100, s[2:3], v100, 0, s[2:3]
	v_addc_co_u32_e64 v101, s[4:5], v101, 0, s[4:5]
	v_addc_co_u32_e64 v100, s[6:7], v100, 0, s[6:7]
	v_addc_co_u32_e64 v101, s[8:9], v101, 0, s[8:9]
	v_addc_co_u32_e64 v100, s[10:11], v100, 0, s[10:11]
	v_addc_co_u32_e64 v101, s[12:13], v101, 0, s[12:13]
	v_addc_co_u32_e64 v100, s[14:15], v100, 0, s[14:15]
	v_addc_co_u32_e64 v101, s[16:17], v101, 0, s[16:17]
	s_nop 0
	v_add_u32_e32 v100, v100, v101
	s_nop 1
	v_add_u32_dpp v100, v100, v100 quad_perm:[1,0,3,2] row_mask:0xf bank_mask:0xf bound_ctrl:1
	s_nop 1
	v_add_u32_dpp v100, v100, v100 quad_perm:[2,3,0,1] row_mask:0xf bank_mask:0xf bound_ctrl:1
	s_nop 1
	v_add_u32_dpp v100, v100, v100 row_half_mirror row_mask:0xf bank_mask:0xf bound_ctrl:1
	s_nop 1
	v_add_u32_dpp v100, v100, v100 row_mirror row_mask:0xf bank_mask:0xf bound_ctrl:1
	v_mov_b32_e32 v101, v100
	s_nop 1
	v_permlane16_swap_b32_e32 v100, v101
	v_add_u32_e32 v100, v100, v101
	v_mov_b32_e32 v101, v100
	s_nop 1
	v_permlane32_swap_b32_e32 v100, v101
	v_add_u32_e32 v100, v100, v101
	s_nop 0
	v_readfirstlane_b32 s29, v100
	s_cmpk_eq_i32 s29, 0x100
	s_cbranch_scc1 .Lsf1409_hit
	s_cmpk_gt_i32 s29, 0x100
	s_cbranch_scc1 .Lsf1409_up
	s_mov_b32 s22, s27
	s_mov_b32 s21, s29
	s_cmp_eq_u32 s31, 2
	s_cbranch_scc0 .Lsf1409_hd
	s_sub_i32 s26, s23, 0x100
	s_lshr_b32 s26, s26, 1
	s_max_u32 s26, s26, 1
	s_add_i32 s23, s26, 0x100

.LBB0_1655:
	s_and_b64 vcc, exec, s[0:1]
	s_cbranch_vccz .LBB0_1868
	s_waitcnt lgkmcnt(3)
	v_max_u32_e32 v89, v63, v62
	s_waitcnt lgkmcnt(2)
	v_max3_u32 v89, v61, v60, v89
	s_waitcnt lgkmcnt(1)
	v_max3_u32 v89, v59, v58, v89
	s_waitcnt lgkmcnt(0)
	v_max3_u32 v89, v57, v56, v89
	ds_read2st64_b32 v[86:87], v183 offset0:8 offset1:9
	ds_read2st64_b32 v[84:85], v183 offset0:10 offset1:11
	ds_read2st64_b32 v[82:83], v183 offset0:12 offset1:13
	ds_read2st64_b32 v[80:81], v183 offset0:14 offset1:15
	ds_read2st64_b32 v[78:79], v183 offset0:16 offset1:17
	ds_read2st64_b32 v[76:77], v183 offset0:18 offset1:19
	ds_read2st64_b32 v[74:75], v183 offset0:20 offset1:21
	ds_read2st64_b32 v[72:73], v183 offset0:22 offset1:23
	ds_read2st64_b32 v[70:71], v183 offset0:24 offset1:25
	ds_read2st64_b32 v[68:69], v183 offset0:26 offset1:27
	ds_read2st64_b32 v[66:67], v183 offset0:28 offset1:29
	ds_read2st64_b32 v[64:65], v183 offset0:30 offset1:31
	s_waitcnt lgkmcnt(11)
	v_max3_u32 v89, v87, v86, v89
	s_waitcnt lgkmcnt(10)
	v_max3_u32 v89, v85, v84, v89
	s_waitcnt lgkmcnt(9)
	v_max3_u32 v89, v83, v82, v89
	s_waitcnt lgkmcnt(8)
	v_max3_u32 v89, v81, v80, v89
	s_waitcnt lgkmcnt(7)
	v_max3_u32 v89, v79, v78, v89
	s_waitcnt lgkmcnt(6)
	v_max3_u32 v89, v77, v76, v89
	s_waitcnt lgkmcnt(5)
	v_max3_u32 v89, v75, v74, v89
	s_waitcnt lgkmcnt(4)
	v_max3_u32 v89, v73, v72, v89
	s_waitcnt lgkmcnt(3)
	v_max3_u32 v89, v71, v70, v89
	s_waitcnt lgkmcnt(2)
	v_max3_u32 v89, v69, v68, v89
	s_waitcnt lgkmcnt(1)
	v_max3_u32 v89, v67, v66, v89
	s_waitcnt lgkmcnt(0)
	v_max3_u32 v89, v65, v64, v89
	s_nop 1
	v_max_u32_dpp v89, v89, v89 quad_perm:[1,0,3,2] row_mask:0xf bank_mask:0xf bound_ctrl:1
	s_nop 1
	v_max_u32_dpp v89, v89, v89 quad_perm:[2,3,0,1] row_mask:0xf bank_mask:0xf bound_ctrl:1
	s_nop 1
	v_max_u32_dpp v89, v89, v89 row_half_mirror row_mask:0xf bank_mask:0xf bound_ctrl:1
	s_nop 1
	v_max_u32_dpp v89, v89, v89 row_mirror row_mask:0xf bank_mask:0xf bound_ctrl:1
	v_mov_b32_e32 v90, v89
	s_nop 1
	v_permlane16_swap_b32_e32 v89, v90
	v_max_u32_e32 v89, v89, v90
	v_mov_b32_e32 v90, v89
	s_nop 1
	v_permlane32_swap_b32_e32 v89, v90
	v_max_u32_e32 v89, v89, v90
	s_nop 0
	v_readfirstlane_b32 s0, v89
	s_and_b32 s7, s0, 0xff800000
	s_lshr_b32 s0, s0, 23
	s_min_u32 s0, s0, 3
	s_mov_b32 s21, 0
	s_add_i32 s5, s0, 1
	s_branch .LBB0_1658

.LBB0_1658:
	v_mov_b32_e32 v90, v199
	v_mov_b32_e32 v91, v199
	s_mov_b32 s4, s7
	v_mov_b32_e32 v89, s7
	v_cmp_ge_u32_e64 s[0:1], v62, v89
	v_cmp_ge_u32_e64 s[2:3], v63, v89
	v_cmp_ge_u32_e64 s[6:7], v60, v89
	v_cmp_ge_u32_e64 s[8:9], v61, v89
	v_cmp_ge_u32_e64 s[10:11], v58, v89
	v_cmp_ge_u32_e64 s[12:13], v59, v89
	v_cmp_ge_u32_e64 s[14:15], v56, v89
	v_cmp_ge_u32_e64 s[16:17], v57, v89
	v_addc_co_u32_e64 v90, s[0:1], v90, 0, s[0:1]
	v_addc_co_u32_e64 v91, s[2:3], v91, 0, s[2:3]
	v_addc_co_u32_e64 v90, s[6:7], v90, 0, s[6:7]
	v_addc_co_u32_e64 v91, s[8:9], v91, 0, s[8:9]
	v_addc_co_u32_e64 v90, s[10:11], v90, 0, s[10:11]
	v_addc_co_u32_e64 v91, s[12:13], v91, 0, s[12:13]
	v_addc_co_u32_e64 v90, s[14:15], v90, 0, s[14:15]
	v_addc_co_u32_e64 v91, s[16:17], v91, 0, s[16:17]
	s_nop 0
	v_cmp_ge_u32_e64 s[0:1], v86, v89
	v_cmp_ge_u32_e64 s[2:3], v87, v89
	v_cmp_ge_u32_e64 s[6:7], v84, v89
	v_cmp_ge_u32_e64 s[8:9], v85, v89
	v_cmp_ge_u32_e64 s[10:11], v82, v89
	v_cmp_ge_u32_e64 s[12:13], v83, v89
	v_cmp_ge_u32_e64 s[14:15], v80, v89
	v_cmp_ge_u32_e64 s[16:17], v81, v89
	v_addc_co_u32_e64 v90, s[0:1], v90, 0, s[0:1]
	v_addc_co_u32_e64 v91, s[2:3], v91, 0, s[2:3]
	v_addc_co_u32_e64 v90, s[6:7], v90, 0, s[6:7]
	v_addc_co_u32_e64 v91, s[8:9], v91, 0, s[8:9]
	v_addc_co_u32_e64 v90, s[10:11], v90, 0, s[10:11]
	v_addc_co_u32_e64 v91, s[12:13], v91, 0, s[12:13]
	v_addc_co_u32_e64 v90, s[14:15], v90, 0, s[14:15]
	v_addc_co_u32_e64 v91, s[16:17], v91, 0, s[16:17]
	s_nop 0
	v_cmp_ge_u32_e64 s[0:1], v78, v89
	v_cmp_ge_u32_e64 s[2:3], v79, v89
	v_cmp_ge_u32_e64 s[6:7], v76, v89
	v_cmp_ge_u32_e64 s[8:9], v77, v89
	v_cmp_ge_u32_e64 s[10:11], v74, v89
	v_cmp_ge_u32_e64 s[12:13], v75, v89
	v_cmp_ge_u32_e64 s[14:15], v72, v89
	v_cmp_ge_u32_e64 s[16:17], v73, v89
	v_addc_co_u32_e64 v90, s[0:1], v90, 0, s[0:1]
	v_addc_co_u32_e64 v91, s[2:3], v91, 0, s[2:3]
	v_addc_co_u32_e64 v90, s[6:7], v90, 0, s[6:7]
	v_addc_co_u32_e64 v91, s[8:9], v91, 0, s[8:9]
	v_addc_co_u32_e64 v90, s[10:11], v90, 0, s[10:11]
	v_addc_co_u32_e64 v91, s[12:13], v91, 0, s[12:13]
	v_addc_co_u32_e64 v90, s[14:15], v90, 0, s[14:15]
	v_addc_co_u32_e64 v91, s[16:17], v91, 0, s[16:17]
	s_nop 0
	v_cmp_ge_u32_e64 s[0:1], v70, v89
	v_cmp_ge_u32_e64 s[2:3], v71, v89
	v_cmp_ge_u32_e64 s[6:7], v68, v89
	v_cmp_ge_u32_e64 s[8:9], v69, v89
	v_cmp_ge_u32_e64 s[10:11], v66, v89
	v_cmp_ge_u32_e64 s[12:13], v67, v89
	v_cmp_ge_u32_e64 s[14:15], v64, v89
	v_cmp_ge_u32_e64 s[16:17], v65, v89
	v_addc_co_u32_e64 v90, s[0:1], v90, 0, s[0:1]
	v_addc_co_u32_e64 v91, s[2:3], v91, 0, s[2:3]
	v_addc_co_u32_e64 v90, s[6:7], v90, 0, s[6:7]
	v_addc_co_u32_e64 v91, s[8:9], v91, 0, s[8:9]
	v_addc_co_u32_e64 v90, s[10:11], v90, 0, s[10:11]
	v_addc_co_u32_e64 v91, s[12:13], v91, 0, s[12:13]
	v_addc_co_u32_e64 v90, s[14:15], v90, 0, s[14:15]
	v_addc_co_u32_e64 v91, s[16:17], v91, 0, s[16:17]
	s_mov_b64 s[0:1], -1
	v_add_u32_e32 v89, v90, v91
	s_mov_b64 s[2:3], -1
	s_nop 0
	v_add_u32_dpp v89, v89, v89 quad_perm:[1,0,3,2] row_mask:0xf bank_mask:0xf bound_ctrl:1
	s_nop 1
	v_add_u32_dpp v89, v89, v89 quad_perm:[2,3,0,1] row_mask:0xf bank_mask:0xf bound_ctrl:1
	s_nop 1
	v_add_u32_dpp v89, v89, v89 row_half_mirror row_mask:0xf bank_mask:0xf bound_ctrl:1
	s_nop 1
	v_add_u32_dpp v89, v89, v89 row_mirror row_mask:0xf bank_mask:0xf bound_ctrl:1
	v_mov_b32_e32 v90, v89
	s_nop 1
	v_permlane16_swap_b32_e32 v89, v90
	v_add_u32_e32 v89, v89, v90
	v_mov_b32_e32 v90, v89
	s_nop 1
	v_permlane32_swap_b32_e32 v89, v90
	v_add_u32_e32 v89, v89, v90
	s_nop 0
	v_readfirstlane_b32 s6, v89
	s_cmpk_lt_i32 s6, 0x100
	s_cbranch_scc0 .LBB0_1657
	s_mov_b32 s21, s6
	s_add_i32 s5, s5, -1
	s_add_i32 s7, s4, 0xff800000
	s_cmp_eq_u32 s5, 0
	s_mov_b64 s[0:1], 0
	s_cselect_b64 s[2:3], -1, 0
	s_branch .LBB0_1657

.Lsf1664_loop:
	s_sub_i32 s25, s22, s20
	s_cmp_lt_u32 s25, 2
	s_cbranch_scc1 .Lsf1664_tie
	s_sub_i32 s26, s23, s21
	s_sub_i32 s27, s23, 0x100
	v_cvt_f32_u32_e32 v92, s25
	v_cvt_f32_u32_e32 v93, s26
	v_cvt_f32_u32_e32 v91, s27
	v_rcp_f32_e32 v93, v93
	v_add_f32_e32 v91, 0.5, v91
	s_nop 0
	v_mul_f32_e32 v92, v92, v93
	v_mul_f32_e32 v91, v91, v92
	v_cvt_u32_f32_e32 v91, v91
	s_nop 0
	v_readfirstlane_b32 s27, v91
	s_sub_i32 s28, s25, 1
	s_max_u32 s27, s27, 1
	s_min_u32 s27, s27, s28
	s_add_i32 s27, s20, s27
	v_mov_b32_e32 v91, s27
	v_mov_b32_e32 v92, v199
	v_mov_b32_e32 v93, v199
	v_cmp_ge_u32_e64 s[2:3], v62, v91
	v_cmp_ge_u32_e64 s[4:5], v63, v91
	v_cmp_ge_u32_e64 s[6:7], v60, v91
	v_cmp_ge_u32_e64 s[8:9], v61, v91
	v_cmp_ge_u32_e64 s[10:11], v58, v91
	v_cmp_ge_u32_e64 s[12:13], v59, v91
	v_cmp_ge_u32_e64 s[14:15], v56, v91
	v_cmp_ge_u32_e64 s[16:17], v57, v91
	v_addc_co_u32_e64 v92, s[2:3], v92, 0, s[2:3]
	v_addc_co_u32_e64 v93, s[4:5], v93, 0, s[4:5]
	v_addc_co_u32_e64 v92, s[6:7], v92, 0, s[6:7]
	v_addc_co_u32_e64 v93, s[8:9], v93, 0, s[8:9]
	v_addc_co_u32_e64 v92, s[10:11], v92, 0, s[10:11]
	v_addc_co_u32_e64 v93, s[12:13], v93, 0, s[12:13]
	v_addc_co_u32_e64 v92, s[14:15], v92, 0, s[14:15]
	v_addc_co_u32_e64 v93, s[16:17], v93, 0, s[16:17]
	s_nop 0
	v_cmp_ge_u32_e64 s[2:3], v86, v91
	v_cmp_ge_u32_e64 s[4:5], v87, v91
	v_cmp_ge_u32_e64 s[6:7], v84, v91
	v_cmp_ge_u32_e64 s[8:9], v85, v91
	v_cmp_ge_u32_e64 s[10:11], v82, v91
	v_cmp_ge_u32_e64 s[12:13], v83, v91
	v_cmp_ge_u32_e64 s[14:15], v80, v91
	v_cmp_ge_u32_e64 s[16:17], v81, v91
	v_addc_co_u32_e64 v92, s[2:3], v92, 0, s[2:3]
	v_addc_co_u32_e64 v93, s[4:5], v93, 0, s[4:5]
	v_addc_co_u32_e64 v92, s[6:7], v92, 0, s[6:7]
	v_addc_co_u32_e64 v93, s[8:9], v93, 0, s[8:9]
	v_addc_co_u32_e64 v92, s[10:11], v92, 0, s[10:11]
	v_addc_co_u32_e64 v93, s[12:13], v93, 0, s[12:13]
	v_addc_co_u32_e64 v92, s[14:15], v92, 0, s[14:15]
	v_addc_co_u32_e64 v93, s[16:17], v93, 0, s[16:17]
	s_nop 0
	v_cmp_ge_u32_e64 s[2:3], v78, v91
	v_cmp_ge_u32_e64 s[4:5], v79, v91
	v_cmp_ge_u32_e64 s[6:7], v76, v91
	v_cmp_ge_u32_e64 s[8:9], v77, v91
	v_cmp_ge_u32_e64 s[10:11], v74, v91
	v_cmp_ge_u32_e64 s[12:13], v75, v91
	v_cmp_ge_u32_e64 s[14:15], v72, v91
	v_cmp_ge_u32_e64 s[16:17], v73, v91
	v_addc_co_u32_e64 v92, s[2:3], v92, 0, s[2:3]
	v_addc_co_u32_e64 v93, s[4:5], v93, 0, s[4:5]
	v_addc_co_u32_e64 v92, s[6:7], v92, 0, s[6:7]
	v_addc_co_u32_e64 v93, s[8:9], v93, 0, s[8:9]
	v_addc_co_u32_e64 v92, s[10:11], v92, 0, s[10:11]
	v_addc_co_u32_e64 v93, s[12:13], v93, 0, s[12:13]
	v_addc_co_u32_e64 v92, s[14:15], v92, 0, s[14:15]
	v_addc_co_u32_e64 v93, s[16:17], v93, 0, s[16:17]
	s_nop 0
	v_cmp_ge_u32_e64 s[2:3], v70, v91
	v_cmp_ge_u32_e64 s[4:5], v71, v91
	v_cmp_ge_u32_e64 s[6:7], v68, v91
	v_cmp_ge_u32_e64 s[8:9], v69, v91
	v_cmp_ge_u32_e64 s[10:11], v66, v91
	v_cmp_ge_u32_e64 s[12:13], v67, v91
	v_cmp_ge_u32_e64 s[14:15], v64, v91
	v_cmp_ge_u32_e64 s[16:17], v65, v91
	v_addc_co_u32_e64 v92, s[2:3], v92, 0, s[2:3]
	v_addc_co_u32_e64 v93, s[4:5], v93, 0, s[4:5]
	v_addc_co_u32_e64 v92, s[6:7], v92, 0, s[6:7]
	v_addc_co_u32_e64 v93, s[8:9], v93, 0, s[8:9]
	v_addc_co_u32_e64 v92, s[10:11], v92, 0, s[10:11]
	v_addc_co_u32_e64 v93, s[12:13], v93, 0, s[12:13]
	v_addc_co_u32_e64 v92, s[14:15], v92, 0, s[14:15]
	v_addc_co_u32_e64 v93, s[16:17], v93, 0, s[16:17]
	s_nop 0
	v_add_u32_e32 v92, v92, v93
	s_nop 1
	v_add_u32_dpp v92, v92, v92 quad_perm:[1,0,3,2] row_mask:0xf bank_mask:0xf bound_ctrl:1
	s_nop 1
	v_add_u32_dpp v92, v92, v92 quad_perm:[2,3,0,1] row_mask:0xf bank_mask:0xf bound_ctrl:1
	s_nop 1
	v_add_u32_dpp v92, v92, v92 row_half_mirror row_mask:0xf bank_mask:0xf bound_ctrl:1
	s_nop 1
	v_add_u32_dpp v92, v92, v92 row_mirror row_mask:0xf bank_mask:0xf bound_ctrl:1
	v_mov_b32_e32 v93, v92
	s_nop 1
	v_permlane16_swap_b32_e32 v92, v93
	v_add_u32_e32 v92, v92, v93
	v_mov_b32_e32 v93, v92
	s_nop 1
	v_permlane32_swap_b32_e32 v92, v93
	v_add_u32_e32 v92, v92, v93
	s_nop 0
	v_readfirstlane_b32 s29, v92
	s_cmpk_eq_i32 s29, 0x100
	s_cbranch_scc1 .Lsf1664_hit
	s_cmpk_gt_i32 s29, 0x100
	s_cbranch_scc1 .Lsf1664_up
	s_mov_b32 s22, s27
	s_mov_b32 s21, s29
	s_cmp_eq_u32 s31, 2
	s_cbranch_scc0 .Lsf1664_hd
	s_sub_i32 s26, s23, 0x100
	s_lshr_b32 s26, s26, 1
	s_max_u32 s26, s26, 1
	s_add_i32 s23, s26, 0x100

.LBB0_1861:
	s_and_b64 vcc, exec, s[0:1]
	s_cbranch_vccz .LBB0_1869
	v_readlane_b32 s0, v254, 52
	s_cmp_gt_i32 s0, 1
	s_mov_b64 s[0:1], -1
	s_cbranch_scc0 .LBB0_2135
	v_readlane_b32 s0, v254, 52
	s_cmp_gt_i32 s0, 2
	s_mov_b64 s[0:1], -1
	s_cbranch_scc0 .LBB0_2024
	s_waitcnt lgkmcnt(3)
	v_max_u32_e32 v80, v63, v62
	s_waitcnt lgkmcnt(2)
	v_max3_u32 v80, v61, v60, v80
	s_waitcnt lgkmcnt(1)
	v_max3_u32 v80, v59, v58, v80
	s_waitcnt lgkmcnt(0)
	v_max3_u32 v80, v57, v56, v80
	ds_read2st64_b32 v[78:79], v183 offset0:8 offset1:9
	ds_read2st64_b32 v[76:77], v183 offset0:10 offset1:11
	ds_read2st64_b32 v[74:75], v183 offset0:12 offset1:13
	ds_read2st64_b32 v[72:73], v183 offset0:14 offset1:15
	ds_read2st64_b32 v[70:71], v183 offset0:16 offset1:17
	ds_read2st64_b32 v[68:69], v183 offset0:18 offset1:19
	ds_read2st64_b32 v[66:67], v183 offset0:20 offset1:21
	ds_read2st64_b32 v[64:65], v183 offset0:22 offset1:23
	s_waitcnt lgkmcnt(7)
	v_max3_u32 v80, v79, v78, v80
	s_waitcnt lgkmcnt(6)
	v_max3_u32 v80, v77, v76, v80
	s_waitcnt lgkmcnt(5)
	v_max3_u32 v80, v75, v74, v80
	s_waitcnt lgkmcnt(4)
	v_max3_u32 v80, v73, v72, v80
	s_waitcnt lgkmcnt(3)
	v_max3_u32 v80, v71, v70, v80
	s_waitcnt lgkmcnt(2)
	v_max3_u32 v80, v69, v68, v80
	s_waitcnt lgkmcnt(1)
	v_max3_u32 v80, v67, v66, v80
	s_waitcnt lgkmcnt(0)
	v_max3_u32 v80, v65, v64, v80
	s_nop 1
	v_max_u32_dpp v80, v80, v80 quad_perm:[1,0,3,2] row_mask:0xf bank_mask:0xf bound_ctrl:1
	s_nop 1
	v_max_u32_dpp v80, v80, v80 quad_perm:[2,3,0,1] row_mask:0xf bank_mask:0xf bound_ctrl:1
	s_nop 1
	v_max_u32_dpp v80, v80, v80 row_half_mirror row_mask:0xf bank_mask:0xf bound_ctrl:1
	s_nop 1
	v_max_u32_dpp v80, v80, v80 row_mirror row_mask:0xf bank_mask:0xf bound_ctrl:1
	v_mov_b32_e32 v81, v80
	s_nop 1
	v_permlane16_swap_b32_e32 v80, v81
	v_max_u32_e32 v80, v80, v81
	v_mov_b32_e32 v81, v80
	s_nop 1
	v_permlane32_swap_b32_e32 v80, v81
	v_max_u32_e32 v80, v80, v81
	s_nop 0
	v_readfirstlane_b32 s0, v80
	s_and_b32 s7, s0, 0xff800000
	s_lshr_b32 s0, s0, 23
	s_min_u32 s0, s0, 3
	s_mov_b32 s21, 0
	s_add_i32 s5, s0, 1
	s_branch .LBB0_1866

.LBB0_1866:
	v_mov_b32_e32 v81, v199
	v_mov_b32_e32 v82, v199
	s_mov_b32 s4, s7
	v_mov_b32_e32 v80, s7
	v_cmp_ge_u32_e64 s[0:1], v62, v80
	v_cmp_ge_u32_e64 s[2:3], v63, v80
	v_cmp_ge_u32_e64 s[6:7], v60, v80
	v_cmp_ge_u32_e64 s[8:9], v61, v80
	v_cmp_ge_u32_e64 s[10:11], v58, v80
	v_cmp_ge_u32_e64 s[12:13], v59, v80
	v_cmp_ge_u32_e64 s[14:15], v56, v80
	v_cmp_ge_u32_e64 s[16:17], v57, v80
	v_addc_co_u32_e64 v81, s[0:1], v81, 0, s[0:1]
	v_addc_co_u32_e64 v82, s[2:3], v82, 0, s[2:3]
	v_addc_co_u32_e64 v81, s[6:7], v81, 0, s[6:7]
	v_addc_co_u32_e64 v82, s[8:9], v82, 0, s[8:9]
	v_addc_co_u32_e64 v81, s[10:11], v81, 0, s[10:11]
	v_addc_co_u32_e64 v82, s[12:13], v82, 0, s[12:13]
	v_addc_co_u32_e64 v81, s[14:15], v81, 0, s[14:15]
	v_addc_co_u32_e64 v82, s[16:17], v82, 0, s[16:17]
	s_nop 0
	v_cmp_ge_u32_e64 s[0:1], v78, v80
	v_cmp_ge_u32_e64 s[2:3], v79, v80
	v_cmp_ge_u32_e64 s[6:7], v76, v80
	v_cmp_ge_u32_e64 s[8:9], v77, v80
	v_cmp_ge_u32_e64 s[10:11], v74, v80
	v_cmp_ge_u32_e64 s[12:13], v75, v80
	v_cmp_ge_u32_e64 s[14:15], v72, v80
	v_cmp_ge_u32_e64 s[16:17], v73, v80
	v_addc_co_u32_e64 v81, s[0:1], v81, 0, s[0:1]
	v_addc_co_u32_e64 v82, s[2:3], v82, 0, s[2:3]
	v_addc_co_u32_e64 v81, s[6:7], v81, 0, s[6:7]
	v_addc_co_u32_e64 v82, s[8:9], v82, 0, s[8:9]
	v_addc_co_u32_e64 v81, s[10:11], v81, 0, s[10:11]
	v_addc_co_u32_e64 v82, s[12:13], v82, 0, s[12:13]
	v_addc_co_u32_e64 v81, s[14:15], v81, 0, s[14:15]
	v_addc_co_u32_e64 v82, s[16:17], v82, 0, s[16:17]
	s_nop 0
	v_cmp_ge_u32_e64 s[0:1], v70, v80
	v_cmp_ge_u32_e64 s[2:3], v71, v80
	v_cmp_ge_u32_e64 s[6:7], v68, v80
	v_cmp_ge_u32_e64 s[8:9], v69, v80
	v_cmp_ge_u32_e64 s[10:11], v66, v80
	v_cmp_ge_u32_e64 s[12:13], v67, v80
	v_cmp_ge_u32_e64 s[14:15], v64, v80
	v_cmp_ge_u32_e64 s[16:17], v65, v80
	v_addc_co_u32_e64 v81, s[0:1], v81, 0, s[0:1]
	v_addc_co_u32_e64 v82, s[2:3], v82, 0, s[2:3]
	v_addc_co_u32_e64 v81, s[6:7], v81, 0, s[6:7]
	v_addc_co_u32_e64 v82, s[8:9], v82, 0, s[8:9]
	v_addc_co_u32_e64 v81, s[10:11], v81, 0, s[10:11]
	v_addc_co_u32_e64 v82, s[12:13], v82, 0, s[12:13]
	v_addc_co_u32_e64 v81, s[14:15], v81, 0, s[14:15]
	v_addc_co_u32_e64 v82, s[16:17], v82, 0, s[16:17]
	s_mov_b64 s[0:1], -1
	v_add_u32_e32 v80, v81, v82
	s_mov_b64 s[2:3], -1
	s_nop 0
	v_add_u32_dpp v80, v80, v80 quad_perm:[1,0,3,2] row_mask:0xf bank_mask:0xf bound_ctrl:1
	s_nop 1
	v_add_u32_dpp v80, v80, v80 quad_perm:[2,3,0,1] row_mask:0xf bank_mask:0xf bound_ctrl:1
	s_nop 1
	v_add_u32_dpp v80, v80, v80 row_half_mirror row_mask:0xf bank_mask:0xf bound_ctrl:1
	s_nop 1
	v_add_u32_dpp v80, v80, v80 row_mirror row_mask:0xf bank_mask:0xf bound_ctrl:1
	v_mov_b32_e32 v81, v80
	s_nop 1
	v_permlane16_swap_b32_e32 v80, v81
	v_add_u32_e32 v80, v80, v81
	v_mov_b32_e32 v81, v80
	s_nop 1
	v_permlane32_swap_b32_e32 v80, v81
	v_add_u32_e32 v80, v80, v81
	s_nop 0
	v_readfirstlane_b32 s6, v80
	s_cmpk_lt_i32 s6, 0x100
	s_cbranch_scc0 .LBB0_1865
	s_mov_b32 s21, s6
	s_add_i32 s5, s5, -1
	s_add_i32 s7, s4, 0xff800000
	s_cmp_eq_u32 s5, 0
	s_mov_b64 s[0:1], 0
	s_cselect_b64 s[2:3], -1, 0
	s_branch .LBB0_1865

.Lsf1874_loop:
	s_sub_i32 s25, s22, s20
	s_cmp_lt_u32 s25, 2
	s_cbranch_scc1 .Lsf1874_tie
	s_sub_i32 s26, s23, s21
	s_sub_i32 s27, s23, 0x100
	v_cvt_f32_u32_e32 v83, s25
	v_cvt_f32_u32_e32 v84, s26
	v_cvt_f32_u32_e32 v82, s27
	v_rcp_f32_e32 v84, v84
	v_add_f32_e32 v82, 0.5, v82
	s_nop 0
	v_mul_f32_e32 v83, v83, v84
	v_mul_f32_e32 v82, v82, v83
	v_cvt_u32_f32_e32 v82, v82
	s_nop 0
	v_readfirstlane_b32 s27, v82
	s_sub_i32 s28, s25, 1
	s_max_u32 s27, s27, 1
	s_min_u32 s27, s27, s28
	s_add_i32 s27, s20, s27
	v_mov_b32_e32 v82, s27
	v_mov_b32_e32 v83, v199
	v_mov_b32_e32 v84, v199
	v_cmp_ge_u32_e64 s[2:3], v62, v82
	v_cmp_ge_u32_e64 s[4:5], v63, v82
	v_cmp_ge_u32_e64 s[6:7], v60, v82
	v_cmp_ge_u32_e64 s[8:9], v61, v82
	v_cmp_ge_u32_e64 s[10:11], v58, v82
	v_cmp_ge_u32_e64 s[12:13], v59, v82
	v_cmp_ge_u32_e64 s[14:15], v56, v82
	v_cmp_ge_u32_e64 s[16:17], v57, v82
	v_addc_co_u32_e64 v83, s[2:3], v83, 0, s[2:3]
	v_addc_co_u32_e64 v84, s[4:5], v84, 0, s[4:5]
	v_addc_co_u32_e64 v83, s[6:7], v83, 0, s[6:7]
	v_addc_co_u32_e64 v84, s[8:9], v84, 0, s[8:9]
	v_addc_co_u32_e64 v83, s[10:11], v83, 0, s[10:11]
	v_addc_co_u32_e64 v84, s[12:13], v84, 0, s[12:13]
	v_addc_co_u32_e64 v83, s[14:15], v83, 0, s[14:15]
	v_addc_co_u32_e64 v84, s[16:17], v84, 0, s[16:17]
	s_nop 0
	v_cmp_ge_u32_e64 s[2:3], v78, v82
	v_cmp_ge_u32_e64 s[4:5], v79, v82
	v_cmp_ge_u32_e64 s[6:7], v76, v82
	v_cmp_ge_u32_e64 s[8:9], v77, v82
	v_cmp_ge_u32_e64 s[10:11], v74, v82
	v_cmp_ge_u32_e64 s[12:13], v75, v82
	v_cmp_ge_u32_e64 s[14:15], v72, v82
	v_cmp_ge_u32_e64 s[16:17], v73, v82
	v_addc_co_u32_e64 v83, s[2:3], v83, 0, s[2:3]
	v_addc_co_u32_e64 v84, s[4:5], v84, 0, s[4:5]
	v_addc_co_u32_e64 v83, s[6:7], v83, 0, s[6:7]
	v_addc_co_u32_e64 v84, s[8:9], v84, 0, s[8:9]
	v_addc_co_u32_e64 v83, s[10:11], v83, 0, s[10:11]
	v_addc_co_u32_e64 v84, s[12:13], v84, 0, s[12:13]
	v_addc_co_u32_e64 v83, s[14:15], v83, 0, s[14:15]
	v_addc_co_u32_e64 v84, s[16:17], v84, 0, s[16:17]
	s_nop 0
	v_cmp_ge_u32_e64 s[2:3], v70, v82
	v_cmp_ge_u32_e64 s[4:5], v71, v82
	v_cmp_ge_u32_e64 s[6:7], v68, v82
	v_cmp_ge_u32_e64 s[8:9], v69, v82
	v_cmp_ge_u32_e64 s[10:11], v66, v82
	v_cmp_ge_u32_e64 s[12:13], v67, v82
	v_cmp_ge_u32_e64 s[14:15], v64, v82
	v_cmp_ge_u32_e64 s[16:17], v65, v82
	v_addc_co_u32_e64 v83, s[2:3], v83, 0, s[2:3]
	v_addc_co_u32_e64 v84, s[4:5], v84, 0, s[4:5]
	v_addc_co_u32_e64 v83, s[6:7], v83, 0, s[6:7]
	v_addc_co_u32_e64 v84, s[8:9], v84, 0, s[8:9]
	v_addc_co_u32_e64 v83, s[10:11], v83, 0, s[10:11]
	v_addc_co_u32_e64 v84, s[12:13], v84, 0, s[12:13]
	v_addc_co_u32_e64 v83, s[14:15], v83, 0, s[14:15]
	v_addc_co_u32_e64 v84, s[16:17], v84, 0, s[16:17]
	s_nop 0
	v_add_u32_e32 v83, v83, v84
	s_nop 1
	v_add_u32_dpp v83, v83, v83 quad_perm:[1,0,3,2] row_mask:0xf bank_mask:0xf bound_ctrl:1
	s_nop 1
	v_add_u32_dpp v83, v83, v83 quad_perm:[2,3,0,1] row_mask:0xf bank_mask:0xf bound_ctrl:1
	s_nop 1
	v_add_u32_dpp v83, v83, v83 row_half_mirror row_mask:0xf bank_mask:0xf bound_ctrl:1
	s_nop 1
	v_add_u32_dpp v83, v83, v83 row_mirror row_mask:0xf bank_mask:0xf bound_ctrl:1
	v_mov_b32_e32 v84, v83
	s_nop 1
	v_permlane16_swap_b32_e32 v83, v84
	v_add_u32_e32 v83, v83, v84
	v_mov_b32_e32 v84, v83
	s_nop 1
	v_permlane32_swap_b32_e32 v83, v84
	v_add_u32_e32 v83, v83, v84
	s_nop 0
	v_readfirstlane_b32 s29, v83
	s_cmpk_eq_i32 s29, 0x100
	s_cbranch_scc1 .Lsf1874_hit
	s_cmpk_gt_i32 s29, 0x100
	s_cbranch_scc1 .Lsf1874_up
	s_mov_b32 s22, s27
	s_mov_b32 s21, s29
	s_cmp_eq_u32 s31, 2
	s_cbranch_scc0 .Lsf1874_hd
	s_sub_i32 s26, s23, 0x100
	s_lshr_b32 s26, s26, 1
	s_max_u32 s26, s26, 1
	s_add_i32 s23, s26, 0x100

.Lsf1874_tie:
	v_mov_b32_e32 v80, s20
	s_mov_b64 s[0:1], 0
	s_branch .LBB0_1875
.Lsf1874_hit:
	v_mov_b32_e32 v80, s27
	s_mov_b64 s[0:1], -1
	s_branch .LBB0_1875

.LBB0_2024:
	s_and_b64 vcc, exec, s[0:1]
	s_cbranch_vccz .LBB0_2134
	s_waitcnt lgkmcnt(3)
	v_max_u32_e32 v72, v63, v62
	s_waitcnt lgkmcnt(2)
	v_max3_u32 v72, v61, v60, v72
	ds_read2st64_b32 v[70:71], v183 offset0:8 offset1:9
	ds_read2st64_b32 v[68:69], v183 offset0:10 offset1:11
	ds_read2st64_b32 v[66:67], v183 offset0:12 offset1:13
	ds_read2st64_b32 v[64:65], v183 offset0:14 offset1:15
	s_waitcnt lgkmcnt(5)
	v_max3_u32 v72, v59, v58, v72
	s_waitcnt lgkmcnt(4)
	v_max3_u32 v72, v57, v56, v72
	s_waitcnt lgkmcnt(3)
	v_max3_u32 v72, v71, v70, v72
	s_waitcnt lgkmcnt(2)
	v_max3_u32 v72, v69, v68, v72
	s_waitcnt lgkmcnt(1)
	v_max3_u32 v72, v67, v66, v72
	s_waitcnt lgkmcnt(0)
	v_max3_u32 v72, v65, v64, v72
	s_nop 1
	v_max_u32_dpp v72, v72, v72 quad_perm:[1,0,3,2] row_mask:0xf bank_mask:0xf bound_ctrl:1
	s_nop 1
	v_max_u32_dpp v72, v72, v72 quad_perm:[2,3,0,1] row_mask:0xf bank_mask:0xf bound_ctrl:1
	s_nop 1
	v_max_u32_dpp v72, v72, v72 row_half_mirror row_mask:0xf bank_mask:0xf bound_ctrl:1
	s_nop 1
	v_max_u32_dpp v72, v72, v72 row_mirror row_mask:0xf bank_mask:0xf bound_ctrl:1
	v_mov_b32_e32 v73, v72
	s_nop 1
	v_permlane16_swap_b32_e32 v72, v73
	v_max_u32_e32 v72, v72, v73
	v_mov_b32_e32 v73, v72
	s_nop 1
	v_permlane32_swap_b32_e32 v72, v73
	v_max_u32_e32 v72, v72, v73
	s_nop 0
	v_readfirstlane_b32 s0, v72
	s_and_b32 s7, s0, 0xff800000
	s_lshr_b32 s0, s0, 23
	s_min_u32 s0, s0, 3
	s_mov_b32 s21, 0
	s_add_i32 s5, s0, 1
	s_branch .LBB0_2027

.LBB0_2027:
	v_mov_b32_e32 v73, v199
	v_mov_b32_e32 v74, v199
	s_mov_b32 s4, s7
	v_mov_b32_e32 v72, s7
	v_cmp_ge_u32_e64 s[0:1], v62, v72
	v_cmp_ge_u32_e64 s[2:3], v63, v72
	v_cmp_ge_u32_e64 s[6:7], v60, v72
	v_cmp_ge_u32_e64 s[8:9], v61, v72
	v_cmp_ge_u32_e64 s[10:11], v58, v72
	v_cmp_ge_u32_e64 s[12:13], v59, v72
	v_cmp_ge_u32_e64 s[14:15], v56, v72
	v_cmp_ge_u32_e64 s[16:17], v57, v72
	v_addc_co_u32_e64 v73, s[0:1], v73, 0, s[0:1]
	v_addc_co_u32_e64 v74, s[2:3], v74, 0, s[2:3]
	v_addc_co_u32_e64 v73, s[6:7], v73, 0, s[6:7]
	v_addc_co_u32_e64 v74, s[8:9], v74, 0, s[8:9]
	v_addc_co_u32_e64 v73, s[10:11], v73, 0, s[10:11]
	v_addc_co_u32_e64 v74, s[12:13], v74, 0, s[12:13]
	v_addc_co_u32_e64 v73, s[14:15], v73, 0, s[14:15]
	v_addc_co_u32_e64 v74, s[16:17], v74, 0, s[16:17]
	s_nop 0
	v_cmp_ge_u32_e64 s[0:1], v70, v72
	v_cmp_ge_u32_e64 s[2:3], v71, v72
	v_cmp_ge_u32_e64 s[6:7], v68, v72
	v_cmp_ge_u32_e64 s[8:9], v69, v72
	v_cmp_ge_u32_e64 s[10:11], v66, v72
	v_cmp_ge_u32_e64 s[12:13], v67, v72
	v_cmp_ge_u32_e64 s[14:15], v64, v72
	v_cmp_ge_u32_e64 s[16:17], v65, v72
	v_addc_co_u32_e64 v73, s[0:1], v73, 0, s[0:1]
	v_addc_co_u32_e64 v74, s[2:3], v74, 0, s[2:3]
	v_addc_co_u32_e64 v73, s[6:7], v73, 0, s[6:7]
	v_addc_co_u32_e64 v74, s[8:9], v74, 0, s[8:9]
	v_addc_co_u32_e64 v73, s[10:11], v73, 0, s[10:11]
	v_addc_co_u32_e64 v74, s[12:13], v74, 0, s[12:13]
	v_addc_co_u32_e64 v73, s[14:15], v73, 0, s[14:15]
	v_addc_co_u32_e64 v74, s[16:17], v74, 0, s[16:17]
	s_mov_b64 s[0:1], -1
	v_add_u32_e32 v72, v73, v74
	s_mov_b64 s[2:3], -1
	s_nop 0
	v_add_u32_dpp v72, v72, v72 quad_perm:[1,0,3,2] row_mask:0xf bank_mask:0xf bound_ctrl:1
	s_nop 1
	v_add_u32_dpp v72, v72, v72 quad_perm:[2,3,0,1] row_mask:0xf bank_mask:0xf bound_ctrl:1
	s_nop 1
	v_add_u32_dpp v72, v72, v72 row_half_mirror row_mask:0xf bank_mask:0xf bound_ctrl:1
	s_nop 1
	v_add_u32_dpp v72, v72, v72 row_mirror row_mask:0xf bank_mask:0xf bound_ctrl:1
	v_mov_b32_e32 v73, v72
	s_nop 1
	v_permlane16_swap_b32_e32 v72, v73
	v_add_u32_e32 v72, v72, v73
	v_mov_b32_e32 v73, v72
	s_nop 1
	v_permlane32_swap_b32_e32 v72, v73
	v_add_u32_e32 v72, v72, v73
	s_nop 0
	v_readfirstlane_b32 s6, v72
	s_cmpk_lt_i32 s6, 0x100
	s_cbranch_scc0 .LBB0_2026
	s_mov_b32 s21, s6
	s_add_i32 s5, s5, -1
	s_add_i32 s7, s4, 0xff800000
	s_cmp_eq_u32 s5, 0
	s_mov_b64 s[0:1], 0
	s_cselect_b64 s[2:3], -1, 0
	s_branch .LBB0_2026

.Lsf2033_loop:
	s_sub_i32 s25, s22, s20
	s_cmp_lt_u32 s25, 2
	s_cbranch_scc1 .Lsf2033_tie
	s_sub_i32 s26, s23, s21
	s_sub_i32 s27, s23, 0x100
	v_cvt_f32_u32_e32 v75, s25
	v_cvt_f32_u32_e32 v76, s26
	v_cvt_f32_u32_e32 v74, s27
	v_rcp_f32_e32 v76, v76
	v_add_f32_e32 v74, 0.5, v74
	s_nop 0
	v_mul_f32_e32 v75, v75, v76
	v_mul_f32_e32 v74, v74, v75
	v_cvt_u32_f32_e32 v74, v74
	s_nop 0
	v_readfirstlane_b32 s27, v74
	s_sub_i32 s28, s25, 1
	s_max_u32 s27, s27, 1
	s_min_u32 s27, s27, s28
	s_add_i32 s27, s20, s27
	v_mov_b32_e32 v74, s27
	v_mov_b32_e32 v75, v199
	v_mov_b32_e32 v76, v199
	v_cmp_ge_u32_e64 s[2:3], v62, v74
	v_cmp_ge_u32_e64 s[4:5], v63, v74
	v_cmp_ge_u32_e64 s[6:7], v60, v74
	v_cmp_ge_u32_e64 s[8:9], v61, v74
	v_cmp_ge_u32_e64 s[10:11], v58, v74
	v_cmp_ge_u32_e64 s[12:13], v59, v74
	v_cmp_ge_u32_e64 s[14:15], v56, v74
	v_cmp_ge_u32_e64 s[16:17], v57, v74
	v_addc_co_u32_e64 v75, s[2:3], v75, 0, s[2:3]
	v_addc_co_u32_e64 v76, s[4:5], v76, 0, s[4:5]
	v_addc_co_u32_e64 v75, s[6:7], v75, 0, s[6:7]
	v_addc_co_u32_e64 v76, s[8:9], v76, 0, s[8:9]
	v_addc_co_u32_e64 v75, s[10:11], v75, 0, s[10:11]
	v_addc_co_u32_e64 v76, s[12:13], v76, 0, s[12:13]
	v_addc_co_u32_e64 v75, s[14:15], v75, 0, s[14:15]
	v_addc_co_u32_e64 v76, s[16:17], v76, 0, s[16:17]
	s_nop 0
	v_cmp_ge_u32_e64 s[2:3], v70, v74
	v_cmp_ge_u32_e64 s[4:5], v71, v74
	v_cmp_ge_u32_e64 s[6:7], v68, v74
	v_cmp_ge_u32_e64 s[8:9], v69, v74
	v_cmp_ge_u32_e64 s[10:11], v66, v74
	v_cmp_ge_u32_e64 s[12:13], v67, v74
	v_cmp_ge_u32_e64 s[14:15], v64, v74
	v_cmp_ge_u32_e64 s[16:17], v65, v74
	v_addc_co_u32_e64 v75, s[2:3], v75, 0, s[2:3]
	v_addc_co_u32_e64 v76, s[4:5], v76, 0, s[4:5]
	v_addc_co_u32_e64 v75, s[6:7], v75, 0, s[6:7]
	v_addc_co_u32_e64 v76, s[8:9], v76, 0, s[8:9]
	v_addc_co_u32_e64 v75, s[10:11], v75, 0, s[10:11]
	v_addc_co_u32_e64 v76, s[12:13], v76, 0, s[12:13]
	v_addc_co_u32_e64 v75, s[14:15], v75, 0, s[14:15]
	v_addc_co_u32_e64 v76, s[16:17], v76, 0, s[16:17]
	s_nop 0
	v_add_u32_e32 v75, v75, v76
	s_nop 1
	v_add_u32_dpp v75, v75, v75 quad_perm:[1,0,3,2] row_mask:0xf bank_mask:0xf bound_ctrl:1
	s_nop 1
	v_add_u32_dpp v75, v75, v75 quad_perm:[2,3,0,1] row_mask:0xf bank_mask:0xf bound_ctrl:1
	s_nop 1
	v_add_u32_dpp v75, v75, v75 row_half_mirror row_mask:0xf bank_mask:0xf bound_ctrl:1
	s_nop 1
	v_add_u32_dpp v75, v75, v75 row_mirror row_mask:0xf bank_mask:0xf bound_ctrl:1
	v_mov_b32_e32 v76, v75
	s_nop 1
	v_permlane16_swap_b32_e32 v75, v76
	v_add_u32_e32 v75, v75, v76
	v_mov_b32_e32 v76, v75
	s_nop 1
	v_permlane32_swap_b32_e32 v75, v76
	v_add_u32_e32 v75, v75, v76
	s_nop 0
	v_readfirstlane_b32 s29, v75
	s_cmpk_eq_i32 s29, 0x100
	s_cbranch_scc1 .Lsf2033_hit
	s_cmpk_gt_i32 s29, 0x100
	s_cbranch_scc1 .Lsf2033_up
	s_mov_b32 s22, s27
	s_mov_b32 s21, s29
	s_cmp_eq_u32 s31, 2
	s_cbranch_scc0 .Lsf2033_hd
	s_sub_i32 s26, s23, 0x100
	s_lshr_b32 s26, s26, 1
	s_max_u32 s26, s26, 1
	s_add_i32 s23, s26, 0x100

.Lsf2033_tie:
	v_mov_b32_e32 v72, s20
	s_mov_b64 s[0:1], 0
	s_branch .LBB0_2034
.Lsf2033_hit:
	v_mov_b32_e32 v72, s27
	s_mov_b64 s[0:1], -1
	s_branch .LBB0_2034

.LBB0_2137:
	s_nop 0
	v_readlane_b32 s0, v254, 54
	v_readlane_b32 s1, v254, 55
	s_waitcnt lgkmcnt(3)
	v_max_u32_e32 v64, v63, v62
	s_and_b64 vcc, exec, s[0:1]
	s_waitcnt lgkmcnt(2)
	v_max3_u32 v89, v61, v60, v64
	s_cbranch_vccz .LBB0_2536
	s_waitcnt lgkmcnt(1)
	v_max3_u32 v122, v59, v58, v89
	s_waitcnt lgkmcnt(0)
	v_max3_u32 v122, v57, v56, v122
	ds_read2st64_b32 v[120:121], v183 offset0:8 offset1:9
	ds_read2st64_b32 v[118:119], v183 offset0:10 offset1:11
	ds_read2st64_b32 v[116:117], v183 offset0:12 offset1:13
	ds_read2st64_b32 v[114:115], v183 offset0:14 offset1:15
	ds_read2st64_b32 v[112:113], v183 offset0:16 offset1:17
	ds_read2st64_b32 v[110:111], v183 offset0:18 offset1:19
	ds_read2st64_b32 v[108:109], v183 offset0:20 offset1:21
	ds_read2st64_b32 v[106:107], v183 offset0:22 offset1:23
	ds_read2st64_b32 v[104:105], v183 offset0:24 offset1:25
	ds_read2st64_b32 v[102:103], v183 offset0:26 offset1:27
	ds_read2st64_b32 v[100:101], v183 offset0:28 offset1:29
	ds_read2st64_b32 v[98:99], v183 offset0:30 offset1:31
	ds_read2st64_b32 v[96:97], v183 offset0:32 offset1:33
	ds_read2st64_b32 v[94:95], v183 offset0:34 offset1:35
	ds_read2st64_b32 v[92:93], v183 offset0:36 offset1:37
	ds_read2st64_b32 v[90:91], v183 offset0:38 offset1:39
	ds_read2st64_b32 v[86:87], v183 offset0:40 offset1:41
	ds_read2st64_b32 v[84:85], v183 offset0:42 offset1:43
	ds_read2st64_b32 v[82:83], v183 offset0:44 offset1:45
	ds_read2st64_b32 v[80:81], v183 offset0:46 offset1:47
	ds_read2st64_b32 v[78:79], v183 offset0:48 offset1:49
	ds_read2st64_b32 v[76:77], v183 offset0:50 offset1:51
	ds_read2st64_b32 v[74:75], v183 offset0:52 offset1:53
	ds_read2st64_b32 v[72:73], v183 offset0:54 offset1:55
	ds_read2st64_b32 v[70:71], v183 offset0:56 offset1:57
	ds_read2st64_b32 v[68:69], v183 offset0:58 offset1:59
	ds_read2st64_b32 v[66:67], v183 offset0:60 offset1:61
	ds_read2st64_b32 v[64:65], v183 offset0:62 offset1:63
	s_waitcnt lgkmcnt(14)
	v_max3_u32 v122, v121, v120, v122
	v_max3_u32 v122, v119, v118, v122
	v_max3_u32 v122, v117, v116, v122
	v_max3_u32 v122, v115, v114, v122
	v_max3_u32 v122, v113, v112, v122
	v_max3_u32 v122, v111, v110, v122
	v_max3_u32 v122, v109, v108, v122
	v_max3_u32 v122, v107, v106, v122
	v_max3_u32 v122, v105, v104, v122
	v_max3_u32 v122, v103, v102, v122
	v_max3_u32 v122, v101, v100, v122
	v_max3_u32 v122, v99, v98, v122
	v_max3_u32 v122, v97, v96, v122
	v_max3_u32 v122, v95, v94, v122
	s_waitcnt lgkmcnt(13)
	v_max3_u32 v122, v93, v92, v122
	s_waitcnt lgkmcnt(12)
	v_max3_u32 v122, v91, v90, v122
	s_waitcnt lgkmcnt(11)
	v_max3_u32 v122, v87, v86, v122
	s_waitcnt lgkmcnt(10)
	v_max3_u32 v122, v85, v84, v122
	s_waitcnt lgkmcnt(9)
	v_max3_u32 v122, v83, v82, v122
	s_waitcnt lgkmcnt(8)
	v_max3_u32 v122, v81, v80, v122
	s_waitcnt lgkmcnt(7)
	v_max3_u32 v122, v79, v78, v122
	s_waitcnt lgkmcnt(6)
	v_max3_u32 v122, v77, v76, v122
	s_waitcnt lgkmcnt(5)
	v_max3_u32 v122, v75, v74, v122
	s_waitcnt lgkmcnt(4)
	v_max3_u32 v122, v73, v72, v122
	s_waitcnt lgkmcnt(3)
	v_max3_u32 v122, v71, v70, v122
	s_waitcnt lgkmcnt(2)
	v_max3_u32 v122, v69, v68, v122
	s_waitcnt lgkmcnt(1)
	v_max3_u32 v122, v67, v66, v122
	s_waitcnt lgkmcnt(0)
	v_max3_u32 v122, v65, v64, v122
	s_nop 1
	v_max_u32_dpp v122, v122, v122 quad_perm:[1,0,3,2] row_mask:0xf bank_mask:0xf bound_ctrl:1
	s_nop 1
	v_max_u32_dpp v122, v122, v122 quad_perm:[2,3,0,1] row_mask:0xf bank_mask:0xf bound_ctrl:1
	s_nop 1
	v_max_u32_dpp v122, v122, v122 row_half_mirror row_mask:0xf bank_mask:0xf bound_ctrl:1
	s_nop 1
	v_max_u32_dpp v122, v122, v122 row_mirror row_mask:0xf bank_mask:0xf bound_ctrl:1
	v_mov_b32_e32 v123, v122
	s_nop 1
	v_permlane16_swap_b32_e32 v122, v123
	v_max_u32_e32 v122, v122, v123
	v_mov_b32_e32 v123, v122
	s_nop 1
	v_permlane32_swap_b32_e32 v122, v123
	v_max_u32_e32 v122, v122, v123
	s_nop 0
	v_readfirstlane_b32 s0, v122
	s_and_b32 s7, s0, 0xff800000
	s_lshr_b32 s0, s0, 23
	s_min_u32 s0, s0, 3
	s_mov_b32 s21, 0
	s_add_i32 s5, s0, 1
	s_branch .LBB0_2140

.LBB0_2140:
	v_mov_b32_e32 v123, v199
	v_mov_b32_e32 v124, v199
	s_mov_b32 s4, s7
	v_mov_b32_e32 v122, s7
	v_cmp_ge_u32_e64 s[0:1], v62, v122
	v_cmp_ge_u32_e64 s[2:3], v63, v122
	v_cmp_ge_u32_e64 s[6:7], v60, v122
	v_cmp_ge_u32_e64 s[8:9], v61, v122
	v_cmp_ge_u32_e64 s[10:11], v58, v122
	v_cmp_ge_u32_e64 s[12:13], v59, v122
	v_cmp_ge_u32_e64 s[14:15], v56, v122
	v_cmp_ge_u32_e64 s[16:17], v57, v122
	v_addc_co_u32_e64 v123, s[0:1], v123, 0, s[0:1]
	v_addc_co_u32_e64 v124, s[2:3], v124, 0, s[2:3]
	v_addc_co_u32_e64 v123, s[6:7], v123, 0, s[6:7]
	v_addc_co_u32_e64 v124, s[8:9], v124, 0, s[8:9]
	v_addc_co_u32_e64 v123, s[10:11], v123, 0, s[10:11]
	v_addc_co_u32_e64 v124, s[12:13], v124, 0, s[12:13]
	v_addc_co_u32_e64 v123, s[14:15], v123, 0, s[14:15]
	v_addc_co_u32_e64 v124, s[16:17], v124, 0, s[16:17]
	s_nop 0
	v_cmp_ge_u32_e64 s[0:1], v120, v122
	v_cmp_ge_u32_e64 s[2:3], v121, v122
	v_cmp_ge_u32_e64 s[6:7], v118, v122
	v_cmp_ge_u32_e64 s[8:9], v119, v122
	v_cmp_ge_u32_e64 s[10:11], v116, v122
	v_cmp_ge_u32_e64 s[12:13], v117, v122
	v_cmp_ge_u32_e64 s[14:15], v114, v122
	v_cmp_ge_u32_e64 s[16:17], v115, v122
	v_addc_co_u32_e64 v123, s[0:1], v123, 0, s[0:1]
	v_addc_co_u32_e64 v124, s[2:3], v124, 0, s[2:3]
	v_addc_co_u32_e64 v123, s[6:7], v123, 0, s[6:7]
	v_addc_co_u32_e64 v124, s[8:9], v124, 0, s[8:9]
	v_addc_co_u32_e64 v123, s[10:11], v123, 0, s[10:11]
	v_addc_co_u32_e64 v124, s[12:13], v124, 0, s[12:13]
	v_addc_co_u32_e64 v123, s[14:15], v123, 0, s[14:15]
	v_addc_co_u32_e64 v124, s[16:17], v124, 0, s[16:17]
	s_nop 0
	v_cmp_ge_u32_e64 s[0:1], v112, v122
	v_cmp_ge_u32_e64 s[2:3], v113, v122
	v_cmp_ge_u32_e64 s[6:7], v110, v122
	v_cmp_ge_u32_e64 s[8:9], v111, v122
	v_cmp_ge_u32_e64 s[10:11], v108, v122
	v_cmp_ge_u32_e64 s[12:13], v109, v122
	v_cmp_ge_u32_e64 s[14:15], v106, v122
	v_cmp_ge_u32_e64 s[16:17], v107, v122
	v_addc_co_u32_e64 v123, s[0:1], v123, 0, s[0:1]
	v_addc_co_u32_e64 v124, s[2:3], v124, 0, s[2:3]
	v_addc_co_u32_e64 v123, s[6:7], v123, 0, s[6:7]
	v_addc_co_u32_e64 v124, s[8:9], v124, 0, s[8:9]
	v_addc_co_u32_e64 v123, s[10:11], v123, 0, s[10:11]
	v_addc_co_u32_e64 v124, s[12:13], v124, 0, s[12:13]
	v_addc_co_u32_e64 v123, s[14:15], v123, 0, s[14:15]
	v_addc_co_u32_e64 v124, s[16:17], v124, 0, s[16:17]
	s_nop 0
	v_cmp_ge_u32_e64 s[0:1], v104, v122
	v_cmp_ge_u32_e64 s[2:3], v105, v122
	v_cmp_ge_u32_e64 s[6:7], v102, v122
	v_cmp_ge_u32_e64 s[8:9], v103, v122
	v_cmp_ge_u32_e64 s[10:11], v100, v122
	v_cmp_ge_u32_e64 s[12:13], v101, v122
	v_cmp_ge_u32_e64 s[14:15], v98, v122
	v_cmp_ge_u32_e64 s[16:17], v99, v122
	v_addc_co_u32_e64 v123, s[0:1], v123, 0, s[0:1]
	v_addc_co_u32_e64 v124, s[2:3], v124, 0, s[2:3]
	v_addc_co_u32_e64 v123, s[6:7], v123, 0, s[6:7]
	v_addc_co_u32_e64 v124, s[8:9], v124, 0, s[8:9]
	v_addc_co_u32_e64 v123, s[10:11], v123, 0, s[10:11]
	v_addc_co_u32_e64 v124, s[12:13], v124, 0, s[12:13]
	v_addc_co_u32_e64 v123, s[14:15], v123, 0, s[14:15]
	v_addc_co_u32_e64 v124, s[16:17], v124, 0, s[16:17]
	s_nop 0
	v_cmp_ge_u32_e64 s[0:1], v96, v122
	v_cmp_ge_u32_e64 s[2:3], v97, v122
	v_cmp_ge_u32_e64 s[6:7], v94, v122
	v_cmp_ge_u32_e64 s[8:9], v95, v122
	v_cmp_ge_u32_e64 s[10:11], v92, v122
	v_cmp_ge_u32_e64 s[12:13], v93, v122
	v_cmp_ge_u32_e64 s[14:15], v90, v122
	v_cmp_ge_u32_e64 s[16:17], v91, v122
	v_addc_co_u32_e64 v123, s[0:1], v123, 0, s[0:1]
	v_addc_co_u32_e64 v124, s[2:3], v124, 0, s[2:3]
	v_addc_co_u32_e64 v123, s[6:7], v123, 0, s[6:7]
	v_addc_co_u32_e64 v124, s[8:9], v124, 0, s[8:9]
	v_addc_co_u32_e64 v123, s[10:11], v123, 0, s[10:11]
	v_addc_co_u32_e64 v124, s[12:13], v124, 0, s[12:13]
	v_addc_co_u32_e64 v123, s[14:15], v123, 0, s[14:15]
	v_addc_co_u32_e64 v124, s[16:17], v124, 0, s[16:17]
	s_nop 0
	v_cmp_ge_u32_e64 s[0:1], v86, v122
	v_cmp_ge_u32_e64 s[2:3], v87, v122
	v_cmp_ge_u32_e64 s[6:7], v84, v122
	v_cmp_ge_u32_e64 s[8:9], v85, v122
	v_cmp_ge_u32_e64 s[10:11], v82, v122
	v_cmp_ge_u32_e64 s[12:13], v83, v122
	v_cmp_ge_u32_e64 s[14:15], v80, v122
	v_cmp_ge_u32_e64 s[16:17], v81, v122
	v_addc_co_u32_e64 v123, s[0:1], v123, 0, s[0:1]
	v_addc_co_u32_e64 v124, s[2:3], v124, 0, s[2:3]
	v_addc_co_u32_e64 v123, s[6:7], v123, 0, s[6:7]
	v_addc_co_u32_e64 v124, s[8:9], v124, 0, s[8:9]
	v_addc_co_u32_e64 v123, s[10:11], v123, 0, s[10:11]
	v_addc_co_u32_e64 v124, s[12:13], v124, 0, s[12:13]
	v_addc_co_u32_e64 v123, s[14:15], v123, 0, s[14:15]
	v_addc_co_u32_e64 v124, s[16:17], v124, 0, s[16:17]
	s_nop 0
	v_cmp_ge_u32_e64 s[0:1], v78, v122
	v_cmp_ge_u32_e64 s[2:3], v79, v122
	v_cmp_ge_u32_e64 s[6:7], v76, v122
	v_cmp_ge_u32_e64 s[8:9], v77, v122
	v_cmp_ge_u32_e64 s[10:11], v74, v122
	v_cmp_ge_u32_e64 s[12:13], v75, v122
	v_cmp_ge_u32_e64 s[14:15], v72, v122
	v_cmp_ge_u32_e64 s[16:17], v73, v122
	v_addc_co_u32_e64 v123, s[0:1], v123, 0, s[0:1]
	v_addc_co_u32_e64 v124, s[2:3], v124, 0, s[2:3]
	v_addc_co_u32_e64 v123, s[6:7], v123, 0, s[6:7]
	v_addc_co_u32_e64 v124, s[8:9], v124, 0, s[8:9]
	v_addc_co_u32_e64 v123, s[10:11], v123, 0, s[10:11]
	v_addc_co_u32_e64 v124, s[12:13], v124, 0, s[12:13]
	v_addc_co_u32_e64 v123, s[14:15], v123, 0, s[14:15]
	v_addc_co_u32_e64 v124, s[16:17], v124, 0, s[16:17]
	s_nop 0
	v_cmp_ge_u32_e64 s[0:1], v70, v122
	v_cmp_ge_u32_e64 s[2:3], v71, v122
	v_cmp_ge_u32_e64 s[6:7], v68, v122
	v_cmp_ge_u32_e64 s[8:9], v69, v122
	v_cmp_ge_u32_e64 s[10:11], v66, v122
	v_cmp_ge_u32_e64 s[12:13], v67, v122
	v_cmp_ge_u32_e64 s[14:15], v64, v122
	v_cmp_ge_u32_e64 s[16:17], v65, v122
	v_addc_co_u32_e64 v123, s[0:1], v123, 0, s[0:1]
	v_addc_co_u32_e64 v124, s[2:3], v124, 0, s[2:3]
	v_addc_co_u32_e64 v123, s[6:7], v123, 0, s[6:7]
	v_addc_co_u32_e64 v124, s[8:9], v124, 0, s[8:9]
	v_addc_co_u32_e64 v123, s[10:11], v123, 0, s[10:11]
	v_addc_co_u32_e64 v124, s[12:13], v124, 0, s[12:13]
	v_addc_co_u32_e64 v123, s[14:15], v123, 0, s[14:15]
	v_addc_co_u32_e64 v124, s[16:17], v124, 0, s[16:17]
	s_mov_b64 s[0:1], -1
	v_add_u32_e32 v122, v123, v124
	s_mov_b64 s[2:3], -1
	s_nop 0
	v_add_u32_dpp v122, v122, v122 quad_perm:[1,0,3,2] row_mask:0xf bank_mask:0xf bound_ctrl:1
	s_nop 1
	v_add_u32_dpp v122, v122, v122 quad_perm:[2,3,0,1] row_mask:0xf bank_mask:0xf bound_ctrl:1
	s_nop 1
	v_add_u32_dpp v122, v122, v122 row_half_mirror row_mask:0xf bank_mask:0xf bound_ctrl:1
	s_nop 1
	v_add_u32_dpp v122, v122, v122 row_mirror row_mask:0xf bank_mask:0xf bound_ctrl:1
	v_mov_b32_e32 v123, v122
	s_nop 1
	v_permlane16_swap_b32_e32 v122, v123
	v_add_u32_e32 v122, v122, v123
	v_mov_b32_e32 v123, v122
	s_nop 1
	v_permlane32_swap_b32_e32 v122, v123
	v_add_u32_e32 v122, v122, v123
	s_nop 0
	v_readfirstlane_b32 s6, v122
	s_cmpk_lt_i32 s6, 0x100
	s_cbranch_scc0 .LBB0_2139
	s_mov_b32 s21, s6
	s_add_i32 s5, s5, -1
	s_add_i32 s7, s4, 0xff800000
	s_cmp_eq_u32 s5, 0
	s_mov_b64 s[0:1], 0
	s_cselect_b64 s[2:3], -1, 0
	s_branch .LBB0_2139

.Lsf2146_loop:
	s_sub_i32 s25, s22, s20
	s_cmp_lt_u32 s25, 2
	s_cbranch_scc1 .Lsf2146_tie
	s_sub_i32 s26, s23, s21
	s_sub_i32 s27, s23, 0x100
	v_cvt_f32_u32_e32 v125, s25
	v_cvt_f32_u32_e32 v126, s26
	v_cvt_f32_u32_e32 v124, s27
	v_rcp_f32_e32 v126, v126
	v_add_f32_e32 v124, 0.5, v124
	s_nop 0
	v_mul_f32_e32 v125, v125, v126
	v_mul_f32_e32 v124, v124, v125
	v_cvt_u32_f32_e32 v124, v124
	s_nop 0
	v_readfirstlane_b32 s27, v124
	s_sub_i32 s28, s25, 1
	s_max_u32 s27, s27, 1
	s_min_u32 s27, s27, s28
	s_add_i32 s27, s20, s27
	v_mov_b32_e32 v124, s27
	v_mov_b32_e32 v125, v199
	v_mov_b32_e32 v126, v199
	v_cmp_ge_u32_e64 s[2:3], v62, v124
	v_cmp_ge_u32_e64 s[4:5], v63, v124
	v_cmp_ge_u32_e64 s[6:7], v60, v124
	v_cmp_ge_u32_e64 s[8:9], v61, v124
	v_cmp_ge_u32_e64 s[10:11], v58, v124
	v_cmp_ge_u32_e64 s[12:13], v59, v124
	v_cmp_ge_u32_e64 s[14:15], v56, v124
	v_cmp_ge_u32_e64 s[16:17], v57, v124
	v_addc_co_u32_e64 v125, s[2:3], v125, 0, s[2:3]
	v_addc_co_u32_e64 v126, s[4:5], v126, 0, s[4:5]
	v_addc_co_u32_e64 v125, s[6:7], v125, 0, s[6:7]
	v_addc_co_u32_e64 v126, s[8:9], v126, 0, s[8:9]
	v_addc_co_u32_e64 v125, s[10:11], v125, 0, s[10:11]
	v_addc_co_u32_e64 v126, s[12:13], v126, 0, s[12:13]
	v_addc_co_u32_e64 v125, s[14:15], v125, 0, s[14:15]
	v_addc_co_u32_e64 v126, s[16:17], v126, 0, s[16:17]
	s_nop 0
	v_cmp_ge_u32_e64 s[2:3], v120, v124
	v_cmp_ge_u32_e64 s[4:5], v121, v124
	v_cmp_ge_u32_e64 s[6:7], v118, v124
	v_cmp_ge_u32_e64 s[8:9], v119, v124
	v_cmp_ge_u32_e64 s[10:11], v116, v124
	v_cmp_ge_u32_e64 s[12:13], v117, v124
	v_cmp_ge_u32_e64 s[14:15], v114, v124
	v_cmp_ge_u32_e64 s[16:17], v115, v124
	v_addc_co_u32_e64 v125, s[2:3], v125, 0, s[2:3]
	v_addc_co_u32_e64 v126, s[4:5], v126, 0, s[4:5]
	v_addc_co_u32_e64 v125, s[6:7], v125, 0, s[6:7]
	v_addc_co_u32_e64 v126, s[8:9], v126, 0, s[8:9]
	v_addc_co_u32_e64 v125, s[10:11], v125, 0, s[10:11]
	v_addc_co_u32_e64 v126, s[12:13], v126, 0, s[12:13]
	v_addc_co_u32_e64 v125, s[14:15], v125, 0, s[14:15]
	v_addc_co_u32_e64 v126, s[16:17], v126, 0, s[16:17]
	s_nop 0
	v_cmp_ge_u32_e64 s[2:3], v112, v124
	v_cmp_ge_u32_e64 s[4:5], v113, v124
	v_cmp_ge_u32_e64 s[6:7], v110, v124
	v_cmp_ge_u32_e64 s[8:9], v111, v124
	v_cmp_ge_u32_e64 s[10:11], v108, v124
	v_cmp_ge_u32_e64 s[12:13], v109, v124
	v_cmp_ge_u32_e64 s[14:15], v106, v124
	v_cmp_ge_u32_e64 s[16:17], v107, v124
	v_addc_co_u32_e64 v125, s[2:3], v125, 0, s[2:3]
	v_addc_co_u32_e64 v126, s[4:5], v126, 0, s[4:5]
	v_addc_co_u32_e64 v125, s[6:7], v125, 0, s[6:7]
	v_addc_co_u32_e64 v126, s[8:9], v126, 0, s[8:9]
	v_addc_co_u32_e64 v125, s[10:11], v125, 0, s[10:11]
	v_addc_co_u32_e64 v126, s[12:13], v126, 0, s[12:13]
	v_addc_co_u32_e64 v125, s[14:15], v125, 0, s[14:15]
	v_addc_co_u32_e64 v126, s[16:17], v126, 0, s[16:17]
	s_nop 0
	v_cmp_ge_u32_e64 s[2:3], v104, v124
	v_cmp_ge_u32_e64 s[4:5], v105, v124
	v_cmp_ge_u32_e64 s[6:7], v102, v124
	v_cmp_ge_u32_e64 s[8:9], v103, v124
	v_cmp_ge_u32_e64 s[10:11], v100, v124
	v_cmp_ge_u32_e64 s[12:13], v101, v124
	v_cmp_ge_u32_e64 s[14:15], v98, v124
	v_cmp_ge_u32_e64 s[16:17], v99, v124
	v_addc_co_u32_e64 v125, s[2:3], v125, 0, s[2:3]
	v_addc_co_u32_e64 v126, s[4:5], v126, 0, s[4:5]
	v_addc_co_u32_e64 v125, s[6:7], v125, 0, s[6:7]
	v_addc_co_u32_e64 v126, s[8:9], v126, 0, s[8:9]
	v_addc_co_u32_e64 v125, s[10:11], v125, 0, s[10:11]
	v_addc_co_u32_e64 v126, s[12:13], v126, 0, s[12:13]
	v_addc_co_u32_e64 v125, s[14:15], v125, 0, s[14:15]
	v_addc_co_u32_e64 v126, s[16:17], v126, 0, s[16:17]
	s_nop 0
	v_cmp_ge_u32_e64 s[2:3], v96, v124
	v_cmp_ge_u32_e64 s[4:5], v97, v124
	v_cmp_ge_u32_e64 s[6:7], v94, v124
	v_cmp_ge_u32_e64 s[8:9], v95, v124
	v_cmp_ge_u32_e64 s[10:11], v92, v124
	v_cmp_ge_u32_e64 s[12:13], v93, v124
	v_cmp_ge_u32_e64 s[14:15], v90, v124
	v_cmp_ge_u32_e64 s[16:17], v91, v124
	v_addc_co_u32_e64 v125, s[2:3], v125, 0, s[2:3]
	v_addc_co_u32_e64 v126, s[4:5], v126, 0, s[4:5]
	v_addc_co_u32_e64 v125, s[6:7], v125, 0, s[6:7]
	v_addc_co_u32_e64 v126, s[8:9], v126, 0, s[8:9]
	v_addc_co_u32_e64 v125, s[10:11], v125, 0, s[10:11]
	v_addc_co_u32_e64 v126, s[12:13], v126, 0, s[12:13]
	v_addc_co_u32_e64 v125, s[14:15], v125, 0, s[14:15]
	v_addc_co_u32_e64 v126, s[16:17], v126, 0, s[16:17]
	s_nop 0
	v_cmp_ge_u32_e64 s[2:3], v86, v124
	v_cmp_ge_u32_e64 s[4:5], v87, v124
	v_cmp_ge_u32_e64 s[6:7], v84, v124
	v_cmp_ge_u32_e64 s[8:9], v85, v124
	v_cmp_ge_u32_e64 s[10:11], v82, v124
	v_cmp_ge_u32_e64 s[12:13], v83, v124
	v_cmp_ge_u32_e64 s[14:15], v80, v124
	v_cmp_ge_u32_e64 s[16:17], v81, v124
	v_addc_co_u32_e64 v125, s[2:3], v125, 0, s[2:3]
	v_addc_co_u32_e64 v126, s[4:5], v126, 0, s[4:5]
	v_addc_co_u32_e64 v125, s[6:7], v125, 0, s[6:7]
	v_addc_co_u32_e64 v126, s[8:9], v126, 0, s[8:9]
	v_addc_co_u32_e64 v125, s[10:11], v125, 0, s[10:11]
	v_addc_co_u32_e64 v126, s[12:13], v126, 0, s[12:13]
	v_addc_co_u32_e64 v125, s[14:15], v125, 0, s[14:15]
	v_addc_co_u32_e64 v126, s[16:17], v126, 0, s[16:17]
	s_nop 0
	v_cmp_ge_u32_e64 s[2:3], v78, v124
	v_cmp_ge_u32_e64 s[4:5], v79, v124
	v_cmp_ge_u32_e64 s[6:7], v76, v124
	v_cmp_ge_u32_e64 s[8:9], v77, v124
	v_cmp_ge_u32_e64 s[10:11], v74, v124
	v_cmp_ge_u32_e64 s[12:13], v75, v124
	v_cmp_ge_u32_e64 s[14:15], v72, v124
	v_cmp_ge_u32_e64 s[16:17], v73, v124
	v_addc_co_u32_e64 v125, s[2:3], v125, 0, s[2:3]
	v_addc_co_u32_e64 v126, s[4:5], v126, 0, s[4:5]
	v_addc_co_u32_e64 v125, s[6:7], v125, 0, s[6:7]
	v_addc_co_u32_e64 v126, s[8:9], v126, 0, s[8:9]
	v_addc_co_u32_e64 v125, s[10:11], v125, 0, s[10:11]
	v_addc_co_u32_e64 v126, s[12:13], v126, 0, s[12:13]
	v_addc_co_u32_e64 v125, s[14:15], v125, 0, s[14:15]
	v_addc_co_u32_e64 v126, s[16:17], v126, 0, s[16:17]
	s_nop 0
	v_cmp_ge_u32_e64 s[2:3], v70, v124
	v_cmp_ge_u32_e64 s[4:5], v71, v124
	v_cmp_ge_u32_e64 s[6:7], v68, v124
	v_cmp_ge_u32_e64 s[8:9], v69, v124
	v_cmp_ge_u32_e64 s[10:11], v66, v124
	v_cmp_ge_u32_e64 s[12:13], v67, v124
	v_cmp_ge_u32_e64 s[14:15], v64, v124
	v_cmp_ge_u32_e64 s[16:17], v65, v124
	v_addc_co_u32_e64 v125, s[2:3], v125, 0, s[2:3]
	v_addc_co_u32_e64 v126, s[4:5], v126, 0, s[4:5]
	v_addc_co_u32_e64 v125, s[6:7], v125, 0, s[6:7]
	v_addc_co_u32_e64 v126, s[8:9], v126, 0, s[8:9]
	v_addc_co_u32_e64 v125, s[10:11], v125, 0, s[10:11]
	v_addc_co_u32_e64 v126, s[12:13], v126, 0, s[12:13]
	v_addc_co_u32_e64 v125, s[14:15], v125, 0, s[14:15]
	v_addc_co_u32_e64 v126, s[16:17], v126, 0, s[16:17]
	s_nop 0
	v_add_u32_e32 v125, v125, v126
	s_nop 1
	v_add_u32_dpp v125, v125, v125 quad_perm:[1,0,3,2] row_mask:0xf bank_mask:0xf bound_ctrl:1
	s_nop 1
	v_add_u32_dpp v125, v125, v125 quad_perm:[2,3,0,1] row_mask:0xf bank_mask:0xf bound_ctrl:1
	s_nop 1
	v_add_u32_dpp v125, v125, v125 row_half_mirror row_mask:0xf bank_mask:0xf bound_ctrl:1
	s_nop 1
	v_add_u32_dpp v125, v125, v125 row_mirror row_mask:0xf bank_mask:0xf bound_ctrl:1
	v_mov_b32_e32 v126, v125
	s_nop 1
	v_permlane16_swap_b32_e32 v125, v126
	v_add_u32_e32 v125, v125, v126
	v_mov_b32_e32 v126, v125
	s_nop 1
	v_permlane32_swap_b32_e32 v125, v126
	v_add_u32_e32 v125, v125, v126
	s_nop 0
	v_readfirstlane_b32 s29, v125
	s_cmpk_eq_i32 s29, 0x100
	s_cbranch_scc1 .Lsf2146_hit
	s_cmpk_gt_i32 s29, 0x100
	s_cbranch_scc1 .Lsf2146_up
	s_mov_b32 s22, s27
	s_mov_b32 s21, s29
	s_cmp_eq_u32 s31, 2
	s_cbranch_scc0 .Lsf2146_hd
	s_sub_i32 s26, s23, 0x100
	s_lshr_b32 s26, s26, 1
	s_max_u32 s26, s26, 1
	s_add_i32 s23, s26, 0x100

.Lsf2146_tie:
	v_mov_b32_e32 v122, s20
	s_mov_b64 s[0:1], 0
	s_branch .LBB0_2147
.Lsf2146_hit:
	v_mov_b32_e32 v122, s27
	s_mov_b64 s[0:1], -1
	s_branch .LBB0_2147

.LBB0_2536:
	s_and_b64 vcc, exec, s[2:3]
	s_cbranch_vccz .LBB0_2598
	s_waitcnt lgkmcnt(1)
	v_max3_u32 v64, v59, v58, v89
	s_waitcnt lgkmcnt(0)
	v_max3_u32 v64, v57, v56, v64
	s_nop 1
	v_max_u32_dpp v64, v64, v64 quad_perm:[1,0,3,2] row_mask:0xf bank_mask:0xf bound_ctrl:1
	s_nop 1
	v_max_u32_dpp v64, v64, v64 quad_perm:[2,3,0,1] row_mask:0xf bank_mask:0xf bound_ctrl:1
	s_nop 1
	v_max_u32_dpp v64, v64, v64 row_half_mirror row_mask:0xf bank_mask:0xf bound_ctrl:1
	s_nop 1
	v_max_u32_dpp v64, v64, v64 row_mirror row_mask:0xf bank_mask:0xf bound_ctrl:1
	v_mov_b32_e32 v65, v64
	s_nop 1
	v_permlane16_swap_b32_e32 v64, v65
	v_max_u32_e32 v64, v64, v65
	v_mov_b32_e32 v65, v64
	s_nop 1
	v_permlane32_swap_b32_e32 v64, v65
	v_max_u32_e32 v64, v64, v65
	s_nop 0
	v_readfirstlane_b32 s0, v64
	s_and_b32 s7, s0, 0xff800000
	s_lshr_b32 s0, s0, 23
	s_min_u32 s0, s0, 3
	s_mov_b32 s21, 0
	s_add_i32 s5, s0, 1
	s_branch .LBB0_2539

.LBB0_2539:
	v_mov_b32_e32 v64, s7
	v_mov_b32_e32 v65, v199
	v_mov_b32_e32 v66, v199
	s_mov_b32 s4, s7
	v_cmp_ge_u32_e64 s[0:1], v62, v64
	v_cmp_ge_u32_e64 s[2:3], v63, v64
	v_cmp_ge_u32_e64 s[6:7], v60, v64
	v_cmp_ge_u32_e64 s[8:9], v61, v64
	v_cmp_ge_u32_e64 s[10:11], v58, v64
	v_cmp_ge_u32_e64 s[12:13], v59, v64
	v_cmp_ge_u32_e64 s[14:15], v56, v64
	v_cmp_ge_u32_e64 s[16:17], v57, v64
	v_addc_co_u32_e64 v65, s[0:1], v65, 0, s[0:1]
	v_addc_co_u32_e64 v66, s[2:3], v66, 0, s[2:3]
	v_addc_co_u32_e64 v65, s[6:7], v65, 0, s[6:7]
	v_addc_co_u32_e64 v66, s[8:9], v66, 0, s[8:9]
	v_addc_co_u32_e64 v65, s[10:11], v65, 0, s[10:11]
	v_addc_co_u32_e64 v66, s[12:13], v66, 0, s[12:13]
	v_addc_co_u32_e64 v65, s[14:15], v65, 0, s[14:15]
	v_addc_co_u32_e64 v66, s[16:17], v66, 0, s[16:17]
	s_mov_b64 s[0:1], -1
	v_add_u32_e32 v64, v65, v66
	s_mov_b64 s[2:3], -1
	s_nop 0
	v_add_u32_dpp v64, v64, v64 quad_perm:[1,0,3,2] row_mask:0xf bank_mask:0xf bound_ctrl:1
	s_nop 1
	v_add_u32_dpp v64, v64, v64 quad_perm:[2,3,0,1] row_mask:0xf bank_mask:0xf bound_ctrl:1
	s_nop 1
	v_add_u32_dpp v64, v64, v64 row_half_mirror row_mask:0xf bank_mask:0xf bound_ctrl:1
	s_nop 1
	v_add_u32_dpp v64, v64, v64 row_mirror row_mask:0xf bank_mask:0xf bound_ctrl:1
	v_mov_b32_e32 v65, v64
	s_nop 1
	v_permlane16_swap_b32_e32 v64, v65
	v_add_u32_e32 v64, v64, v65
	v_mov_b32_e32 v65, v64
	s_nop 1
	v_permlane32_swap_b32_e32 v64, v65
	v_add_u32_e32 v64, v64, v65
	s_nop 0
	v_readfirstlane_b32 s6, v64
	s_cmpk_lt_i32 s6, 0x100
	s_cbranch_scc0 .LBB0_2538
	s_mov_b32 s21, s6
	s_add_i32 s5, s5, -1
	s_add_i32 s7, s4, 0xff800000
	s_cmp_eq_u32 s5, 0
	s_mov_b64 s[0:1], 0
	s_cselect_b64 s[2:3], -1, 0
	s_branch .LBB0_2538

.Lsf2545_loop:
	s_sub_i32 s25, s22, s20
	s_cmp_lt_u32 s25, 2
	s_cbranch_scc1 .Lsf2545_tie
	s_sub_i32 s26, s23, s21
	s_sub_i32 s27, s23, 0x100
	v_cvt_f32_u32_e32 v67, s25
	v_cvt_f32_u32_e32 v68, s26
	v_cvt_f32_u32_e32 v66, s27
	v_rcp_f32_e32 v68, v68
	v_add_f32_e32 v66, 0.5, v66
	s_nop 0
	v_mul_f32_e32 v67, v67, v68
	v_mul_f32_e32 v66, v66, v67
	v_cvt_u32_f32_e32 v66, v66
	s_nop 0
	v_readfirstlane_b32 s27, v66
	s_sub_i32 s28, s25, 1
	s_max_u32 s27, s27, 1
	s_min_u32 s27, s27, s28
	s_add_i32 s27, s20, s27
	v_mov_b32_e32 v66, s27
	v_mov_b32_e32 v67, v199
	v_mov_b32_e32 v68, v199
	v_cmp_ge_u32_e64 s[2:3], v62, v66
	v_cmp_ge_u32_e64 s[4:5], v63, v66
	v_cmp_ge_u32_e64 s[6:7], v60, v66
	v_cmp_ge_u32_e64 s[8:9], v61, v66
	v_cmp_ge_u32_e64 s[10:11], v58, v66
	v_cmp_ge_u32_e64 s[12:13], v59, v66
	v_cmp_ge_u32_e64 s[14:15], v56, v66
	v_cmp_ge_u32_e64 s[16:17], v57, v66
	v_addc_co_u32_e64 v67, s[2:3], v67, 0, s[2:3]
	v_addc_co_u32_e64 v68, s[4:5], v68, 0, s[4:5]
	v_addc_co_u32_e64 v67, s[6:7], v67, 0, s[6:7]
	v_addc_co_u32_e64 v68, s[8:9], v68, 0, s[8:9]
	v_addc_co_u32_e64 v67, s[10:11], v67, 0, s[10:11]
	v_addc_co_u32_e64 v68, s[12:13], v68, 0, s[12:13]
	v_addc_co_u32_e64 v67, s[14:15], v67, 0, s[14:15]
	v_addc_co_u32_e64 v68, s[16:17], v68, 0, s[16:17]
	s_nop 0
	v_add_u32_e32 v67, v67, v68
	s_nop 1
	v_add_u32_dpp v67, v67, v67 quad_perm:[1,0,3,2] row_mask:0xf bank_mask:0xf bound_ctrl:1
	s_nop 1
	v_add_u32_dpp v67, v67, v67 quad_perm:[2,3,0,1] row_mask:0xf bank_mask:0xf bound_ctrl:1
	s_nop 1
	v_add_u32_dpp v67, v67, v67 row_half_mirror row_mask:0xf bank_mask:0xf bound_ctrl:1
	s_nop 1
	v_add_u32_dpp v67, v67, v67 row_mirror row_mask:0xf bank_mask:0xf bound_ctrl:1
	v_mov_b32_e32 v68, v67
	s_nop 1
	v_permlane16_swap_b32_e32 v67, v68
	v_add_u32_e32 v67, v67, v68
	v_mov_b32_e32 v68, v67
	s_nop 1
	v_permlane32_swap_b32_e32 v67, v68
	v_add_u32_e32 v67, v67, v68
	s_nop 0
	v_readfirstlane_b32 s29, v67
	s_cmpk_eq_i32 s29, 0x100
	s_cbranch_scc1 .Lsf2545_hit
	s_cmpk_gt_i32 s29, 0x100
	s_cbranch_scc1 .Lsf2545_up
	s_mov_b32 s22, s27
	s_mov_b32 s21, s29
	s_cmp_eq_u32 s31, 2
	s_cbranch_scc0 .Lsf2545_hd
	s_sub_i32 s26, s23, 0x100
	s_lshr_b32 s26, s26, 1
	s_max_u32 s26, s26, 1
	s_add_i32 s23, s26, 0x100

.Lsf2545_tie:
	v_mov_b32_e32 v64, s20
	s_mov_b64 s[0:1], 0
	s_branch .LBB0_2546
.Lsf2545_hit:
	v_mov_b32_e32 v64, s27
	s_mov_b64 s[0:1], -1
	s_branch .LBB0_2546
